# wave_sum all-reduce: xor-1/2/4/8 steps through DPP moves instead of ds_bpermute round trips (P0 rows, both route phases, combine); stacked on peeled K-loops
# speedup vs baseline: 1.0106x; 1.0106x over previous
.Lp0_nopf:
	v_pk_mul_f32 v[78:79], v[36:37], v[36:37]
	v_pk_mul_f32 v[80:81], v[34:35], v[34:35]
	v_pk_mul_f32 v[82:83], v[40:41], v[40:41]
	v_pk_mul_f32 v[84:85], v[38:39], v[38:39]
	v_mov_b32_e32 v88, v47
	v_mov_b32_e32 v89, v43
	v_mov_b32_e32 v92, v49
	v_mov_b32_e32 v93, v45
	v_mov_b32_e32 v86, v46
	v_mov_b32_e32 v87, v42
	v_mov_b32_e32 v90, v48
	v_mov_b32_e32 v91, v44
	v_pk_mov_b32 v[102:103], v[80:81], v[78:79] op_sel:[1,0]
	v_mov_b32_e32 v81, v79
	v_pk_mov_b32 v[78:79], v[84:85], v[82:83] op_sel:[1,0]
	v_mov_b32_e32 v85, v83
	v_pk_mul_f32 v[82:83], v[88:89], v[88:89]
	v_pk_mul_f32 v[88:89], v[92:93], v[92:93]
	v_pk_fma_f32 v[82:83], v[86:87], v[86:87], v[82:83]
	v_pk_fma_f32 v[86:87], v[90:91], v[90:91], v[88:89]
	v_mul_f32_e32 v94, v55, v55
	v_mul_f32_e32 v96, v57, v57
	v_pk_add_f32 v[80:81], v[102:103], v[80:81]
	v_pk_add_f32 v[82:83], v[82:83], v[86:87]
	v_mul_f32_e32 v1, v52, v52
	v_mul_f32_e32 v101, v53, v53
	v_mul_f32_e32 v106, v51, v51
	v_mul_f32_e32 v107, v50, v50
	v_pk_fma_f32 v[92:93], v[54:55], v[54:55], v[94:95] op_sel_hi:[1,1,0]
	v_pk_fma_f32 v[94:95], v[56:57], v[56:57], v[96:97] op_sel_hi:[1,1,0]
	v_pk_add_f32 v[80:81], v[80:81], v[80:81] op_sel:[0,1] op_sel_hi:[1,0]
	v_pk_add_f32 v[82:83], v[82:83], v[82:83] op_sel:[0,1] op_sel_hi:[1,0]
	v_mov_b32_e32 v93, v1
	v_mov_b32_e32 v95, v101
	v_mov_b32_e32 v81, v106
	v_mov_b32_e32 v83, v107
	v_pk_add_f32 v[78:79], v[78:79], v[84:85]
	v_pk_add_f32 v[84:85], v[92:93], v[94:95]
	v_pk_add_f32 v[80:81], v[82:83], v[80:81]
	v_mul_f32_e32 v98, v63, v63
	v_mul_f32_e32 v100, v65, v65
	v_pk_add_f32 v[80:81], v[80:81], v[84:85]
	v_mul_f32_e32 v104, v60, v60
	v_mul_f32_e32 v105, v61, v61
	v_mul_f32_e32 v108, v59, v59
	v_mul_f32_e32 v109, v58, v58
	v_pk_fma_f32 v[96:97], v[62:63], v[62:63], v[98:99] op_sel_hi:[1,1,0]
	v_pk_fma_f32 v[98:99], v[64:65], v[64:65], v[100:101] op_sel_hi:[1,1,0]
	v_pk_add_f32 v[78:79], v[78:79], v[78:79] op_sel:[0,1] op_sel_hi:[1,0]
	v_pk_add_f32 v[80:81], v[80:81], v[80:81] op_sel:[0,1] op_sel_hi:[1,0]
	v_mov_b32_e32 v97, v104
	v_mov_b32_e32 v99, v105
	v_mov_b32_e32 v79, v108
	v_mov_b32_e32 v81, v109
	v_pk_add_f32 v[86:87], v[96:97], v[98:99]
	v_pk_add_f32 v[78:79], v[80:81], v[78:79]
	s_nop 0
	v_pk_add_f32 v[78:79], v[78:79], v[86:87]
	s_nop 0
	v_add_f32_e32 v1, v78, v79
	s_nop 1
	v_mov_b32_dpp v78, v1 quad_perm:[1,0,3,2] row_mask:0xf bank_mask:0xf
	s_nop 1
	s_waitcnt lgkmcnt(0)
	v_add_f32_e32 v1, v1, v78
	s_nop 1
	v_mov_b32_dpp v78, v1 quad_perm:[2,3,0,1] row_mask:0xf bank_mask:0xf
	s_nop 1
	s_waitcnt lgkmcnt(0)
	v_add_f32_e32 v1, v1, v78
	s_nop 1
	v_mov_b32_dpp v78, v1 row_half_mirror row_mask:0xf bank_mask:0xf
	s_nop 1
	s_waitcnt lgkmcnt(0)
	v_add_f32_e32 v1, v1, v78
	s_nop 1
	v_mov_b32_dpp v78, v1 row_mirror row_mask:0xf bank_mask:0xf
	s_nop 1
	s_waitcnt lgkmcnt(0)
	v_add_f32_e32 v1, v1, v78
	ds_bpermute_b32 v78, v74, v1
	s_waitcnt lgkmcnt(0)
	v_add_f32_e32 v1, v1, v78
	ds_bpermute_b32 v78, v75, v1
	s_waitcnt lgkmcnt(0)
	v_add_f32_e32 v1, v1, v78
	v_fmamk_f32 v1, v1, 0x3a000000, v76
	v_mul_f32_e32 v78, 0x4f800000, v1
	v_cmp_gt_f32_e32 vcc, s2, v1
	s_nop 1
	v_cndmask_b32_e32 v1, v1, v78, vcc
	v_sqrt_f32_e32 v78, v1
	s_nop 0
	v_add_u32_e32 v79, -1, v78
	v_add_u32_e32 v80, 1, v78
	v_fma_f32 v81, -v79, v78, v1
	v_fma_f32 v82, -v80, v78, v1
	v_cmp_ge_f32_e64 s[4:5], 0, v81
	s_nop 1
	v_cndmask_b32_e64 v78, v78, v79, s[4:5]
	v_cmp_lt_f32_e64 s[4:5], 0, v82
	s_nop 1
	v_cndmask_b32_e64 v78, v78, v80, s[4:5]
	v_mul_f32_e32 v79, 0x37800000, v78
	v_cndmask_b32_e32 v78, v78, v79, vcc
	v_cmp_class_f32_e32 vcc, v1, v77
	s_nop 1
	v_cndmask_b32_e32 v1, v78, v1, vcc
	v_div_scale_f32 v78, s[4:5], v1, v1, 1.0
	v_rcp_f32_e32 v80, v78
	v_div_scale_f32 v79, vcc, 1.0, v1, 1.0
	v_fma_f32 v81, -v78, v80, 1.0
	v_fmac_f32_e32 v80, v81, v80
	v_mul_f32_e32 v81, v79, v80
	v_fma_f32 v82, -v78, v81, v79
	v_fmac_f32_e32 v81, v82, v80
	v_fma_f32 v78, -v78, v81, v79
	v_div_fmas_f32 v78, v78, v80, v81
	v_div_fixup_f32 v78, v78, v1, 1.0
	v_pk_mul_f32 v[46:47], v[46:47], v[78:79] op_sel_hi:[1,0]
	v_pk_mul_f32 v[48:49], v[48:49], v[78:79] op_sel_hi:[1,0]
	v_pk_mul_f32 v[42:43], v[42:43], v[78:79] op_sel_hi:[1,0]
	v_pk_mul_f32 v[44:45], v[44:45], v[78:79] op_sel_hi:[1,0]
	v_pk_mul_f32 v[34:35], v[34:35], v[78:79] op_sel_hi:[1,0]
	v_pk_mul_f32 v[36:37], v[36:37], v[78:79] op_sel_hi:[1,0]
	v_pk_mul_f32 v[54:55], v[54:55], v[78:79] op_sel_hi:[1,0]
	v_pk_mul_f32 v[56:57], v[56:57], v[78:79] op_sel_hi:[1,0]
	v_pk_mul_f32 v[50:51], v[50:51], v[78:79] op_sel_hi:[1,0]
	v_pk_mul_f32 v[52:53], v[52:53], v[78:79] op_sel_hi:[1,0]
	v_pk_mul_f32 v[38:39], v[38:39], v[78:79] op_sel_hi:[1,0]
	v_pk_mul_f32 v[40:41], v[40:41], v[78:79] op_sel_hi:[1,0]
	v_pk_mul_f32 v[62:63], v[62:63], v[78:79] op_sel_hi:[1,0]
	v_pk_mul_f32 v[64:65], v[64:65], v[78:79] op_sel_hi:[1,0]
	v_pk_mul_f32 v[58:59], v[58:59], v[78:79] op_sel_hi:[1,0]
	v_pk_mul_f32 v[60:61], v[60:61], v[78:79] op_sel_hi:[1,0]
	v_pk_mul_f32 v[48:49], v[8:9], v[48:49]
	v_pk_mul_f32 v[46:47], v[6:7], v[46:47]
	v_pk_mul_f32 v[42:43], v[2:3], v[42:43]
	v_pk_mul_f32 v[44:45], v[4:5], v[44:45]
	v_pk_mul_f32 v[78:79], v[16:17], v[36:37]
	v_pk_mul_f32 v[80:81], v[14:15], v[34:35]
	v_pk_mul_f32 v[54:55], v[10:11], v[54:55]
	v_pk_mul_f32 v[56:57], v[12:13], v[56:57]
	v_pk_mul_f32 v[52:53], v[20:21], v[52:53]
	v_pk_mul_f32 v[50:51], v[18:19], v[50:51]
	v_pk_mul_f32 v[82:83], v[28:29], v[40:41]
	v_pk_mul_f32 v[84:85], v[26:27], v[38:39]
	v_pk_mul_f32 v[64:65], v[24:25], v[64:65]
	v_pk_mul_f32 v[62:63], v[22:23], v[62:63]
	v_pk_mul_f32 v[60:61], v[32:33], v[60:61]
	v_pk_mul_f32 v[58:59], v[30:31], v[58:59]
	v_cvt_pk_bf16_f32 v34, v46, v47
	v_cvt_pk_bf16_f32 v35, v48, v49
	v_cvt_pk_bf16_f32 v36, v42, v43
	v_cvt_pk_bf16_f32 v37, v44, v45
	v_cvt_pk_bf16_f32 v38, v80, v81
	v_cvt_pk_bf16_f32 v39, v78, v79
	v_cvt_pk_bf16_f32 v40, v54, v55
	v_cvt_pk_bf16_f32 v41, v56, v57
	v_cvt_pk_bf16_f32 v42, v50, v51
	v_cvt_pk_bf16_f32 v43, v52, v53
	v_cvt_pk_bf16_f32 v44, v84, v85
	v_cvt_pk_bf16_f32 v45, v82, v83
	v_cvt_pk_bf16_f32 v46, v62, v63
	v_cvt_pk_bf16_f32 v47, v64, v65
	v_cvt_pk_bf16_f32 v48, v58, v59
	v_cvt_pk_bf16_f32 v49, v60, v61
	global_store_dwordx4 v[68:69], v[34:37], off
	global_store_dwordx4 v[68:69], v[38:41], off offset:1024
	global_store_dwordx4 v[68:69], v[42:45], off offset:2048
	global_store_dwordx4 v[68:69], v[46:49], off offset:3072
	v_lshl_add_u64 v[68:69], v[68:69], 0, s[16:17]
	s_cbranch_scc0 .LBB0_13

.LBB0_592:
	s_lshl_b32 s8, s68, 4
	s_add_i32 s6, s67, s8
	s_ashr_i32 s7, s6, 31
	s_lshl_b64 s[12:13], s[6:7], 13
	v_lshl_add_u64 v[34:35], v[128:129], 0, s[12:13]
	v_lshl_add_u64 v[36:37], v[34:35], 0, s[48:49]
	v_add_co_u32_e32 v36, vcc, 0x1000, v34
	v_and_b32_e32 v1, 64, v220
	s_nop 0
	v_addc_co_u32_e32 v37, vcc, 0, v35, vcc
	v_lshl_add_u64 v[34:35], v[34:35], 0, s[46:47]
	v_xor_b32_e32 v34, 1, v220
	v_add_u32_e32 v1, 64, v1
	s_or_b32 s6, s6, 1
	v_cmp_lt_i32_e32 vcc, v34, v1
	s_ashr_i32 s7, s6, 31
	s_lshl_b64 s[6:7], s[6:7], 13
	v_cndmask_b32_e32 v34, v220, v34, vcc
	v_lshlrev_b32_e32 v218, 2, v34
	v_lshl_add_u64 v[34:35], v[128:129], 0, s[6:7]
	v_add_co_u32_e32 v70, vcc, s34, v34
	v_lshl_add_u64 v[36:37], v[34:35], 0, s[46:47]
	s_nop 0
	v_addc_co_u32_e32 v71, vcc, 0, v35, vcc
	v_lshl_add_u64 v[72:73], v[34:35], 0, s[48:49]
	s_nop 0
	s_add_i32 s8, s8, s66
	s_add_i32 s54, s8, s2
	s_ashr_i32 s55, s54, 31
	s_add_i32 s58, s8, s27
	s_ashr_i32 s59, s58, 31
	s_waitcnt vmcnt(13)
	v_mov_b32_e32 v76, v119
	s_waitcnt vmcnt(12)
	v_mov_b32_e32 v77, v115
	v_mov_b32_e32 v80, v121
	v_mov_b32_e32 v81, v117
	v_mov_b32_e32 v74, v118
	v_mov_b32_e32 v75, v114
	v_mov_b32_e32 v78, v120
	v_mov_b32_e32 v79, v116
	s_waitcnt vmcnt(11)
	v_pk_mul_f32 v[82:83], v[112:113], v[112:113]
	v_pk_mul_f32 v[84:85], v[110:111], v[110:111]
	v_pk_mul_f32 v[76:77], v[76:77], v[76:77]
	v_pk_mul_f32 v[80:81], v[80:81], v[80:81]
	v_pk_mov_b32 v[94:95], v[84:85], v[82:83] op_sel:[1,0]
	v_mov_b32_e32 v85, v83
	v_pk_fma_f32 v[74:75], v[74:75], v[74:75], v[76:77]
	v_pk_fma_f32 v[76:77], v[78:79], v[78:79], v[80:81]
	s_waitcnt vmcnt(10)
	v_mul_f32_e32 v86, v107, v107
	v_mul_f32_e32 v88, v109, v109
	v_pk_add_f32 v[78:79], v[94:95], v[84:85]
	v_pk_add_f32 v[74:75], v[74:75], v[76:77]
	v_pk_fma_f32 v[82:83], v[106:107], v[106:107], v[86:87] op_sel_hi:[1,1,0]
	v_pk_fma_f32 v[86:87], v[108:109], v[108:109], v[88:89] op_sel_hi:[1,1,0]
	s_waitcnt vmcnt(8)
	v_mul_f32_e32 v95, v90, v90
	v_mul_f32_e32 v100, v91, v91
	v_pk_add_f32 v[76:77], v[78:79], v[78:79] op_sel:[0,1] op_sel_hi:[1,0]
	v_pk_add_f32 v[74:75], v[74:75], v[74:75] op_sel:[0,1] op_sel_hi:[1,0]
	v_mul_f32_e32 v83, v92, v92
	v_mul_f32_e32 v87, v93, v93
	s_waitcnt vmcnt(7)
	v_pk_mul_f32 v[80:81], v[68:69], v[68:69]
	v_pk_mul_f32 v[84:85], v[66:67], v[66:67]
	v_mov_b32_e32 v77, v100
	v_mov_b32_e32 v75, v95
	v_pk_mov_b32 v[78:79], v[84:85], v[80:81] op_sel:[1,0]
	v_mov_b32_e32 v85, v81
	v_pk_add_f32 v[82:83], v[82:83], v[86:87]
	v_pk_add_f32 v[74:75], v[74:75], v[76:77]
	s_waitcnt vmcnt(6)
	v_mul_f32_e32 v88, v63, v63
	v_mul_f32_e32 v94, v65, v65
	v_pk_add_f32 v[78:79], v[78:79], v[84:85]
	v_pk_add_f32 v[74:75], v[74:75], v[82:83]
	v_mul_f32_e32 v96, v58, v58
	v_mul_f32_e32 v97, v59, v59
	v_mul_f32_e32 v98, v60, v60
	v_mul_f32_e32 v99, v61, v61
	v_pk_fma_f32 v[80:81], v[62:63], v[62:63], v[88:89] op_sel_hi:[1,1,0]
	v_pk_fma_f32 v[88:89], v[64:65], v[64:65], v[94:95] op_sel_hi:[1,1,0]
	v_pk_add_f32 v[78:79], v[78:79], v[78:79] op_sel:[0,1] op_sel_hi:[1,0]
	v_pk_add_f32 v[74:75], v[74:75], v[74:75] op_sel:[0,1] op_sel_hi:[1,0]
	v_mov_b32_e32 v81, v98
	v_mov_b32_e32 v79, v97
	v_mov_b32_e32 v75, v96
	v_mov_b32_e32 v89, v99
	v_pk_add_f32 v[74:75], v[74:75], v[78:79]
	v_pk_add_f32 v[76:77], v[80:81], v[88:89]
	s_waitcnt vmcnt(0)
	v_mov_b32_e32 v42, v196
	v_mov_b32_e32 v43, v197
	v_mov_b32_e32 v44, v198
	v_mov_b32_e32 v45, v199
	v_mov_b32_e32 v46, v200
	v_mov_b32_e32 v47, v201
	v_mov_b32_e32 v48, v202
	v_mov_b32_e32 v49, v203
	v_mov_b32_e32 v38, v204
	v_mov_b32_e32 v39, v205
	v_mov_b32_e32 v40, v206
	v_mov_b32_e32 v41, v207
	v_mov_b32_e32 v34, v208
	v_mov_b32_e32 v35, v209
	v_mov_b32_e32 v36, v210
	v_mov_b32_e32 v37, v211
	v_mov_b32_e32 v98, v212
	v_mov_b32_e32 v99, v213
	v_mov_b32_e32 v100, v214
	v_mov_b32_e32 v101, v215
	global_load_dwordx4 v[82:85], v[126:127], off
	global_load_dwordx4 v[86:89], v[126:127], off offset:256
	v_pk_add_f32 v[74:75], v[74:75], v[76:77]
	v_xor_b32_e32 v76, 2, v220
	v_add_f32_e32 v74, v74, v75
	s_nop 1
	v_mov_b32_dpp v75, v74 quad_perm:[1,0,3,2] row_mask:0xf bank_mask:0xf
	s_nop 1
	v_cmp_lt_i32_e32 vcc, v76, v1
	s_waitcnt lgkmcnt(0)
	v_add_f32_e32 v74, v74, v75
	v_cndmask_b32_e32 v76, v220, v76, vcc
	v_lshlrev_b32_e32 v225, 2, v76
	s_nop 1
	v_mov_b32_dpp v75, v74 quad_perm:[2,3,0,1] row_mask:0xf bank_mask:0xf
	s_nop 1
	v_xor_b32_e32 v76, 4, v220
	v_cmp_lt_i32_e32 vcc, v76, v1
	s_waitcnt lgkmcnt(0)
	v_add_f32_e32 v74, v74, v75
	v_cndmask_b32_e32 v76, v220, v76, vcc
	v_lshlrev_b32_e32 v230, 2, v76
	s_nop 1
	v_mov_b32_dpp v75, v74 row_half_mirror row_mask:0xf bank_mask:0xf
	s_nop 1
	v_xor_b32_e32 v76, 8, v220
	v_cmp_lt_i32_e32 vcc, v76, v1
	s_waitcnt lgkmcnt(0)
	v_add_f32_e32 v74, v74, v75
	v_cndmask_b32_e32 v76, v220, v76, vcc
	v_lshlrev_b32_e32 v231, 2, v76
	s_nop 1
	v_mov_b32_dpp v75, v74 row_mirror row_mask:0xf bank_mask:0xf
	s_nop 1
	v_xor_b32_e32 v76, 16, v220
	v_cmp_lt_i32_e32 vcc, v76, v1
	s_waitcnt lgkmcnt(0)
	v_add_f32_e32 v74, v74, v75
	v_cndmask_b32_e32 v76, v220, v76, vcc
	v_lshlrev_b32_e32 v232, 2, v76
	ds_bpermute_b32 v75, v232, v74
	v_xor_b32_e32 v76, 32, v220
	v_cmp_lt_i32_e32 vcc, v76, v1
	s_waitcnt lgkmcnt(0)
	v_add_f32_e32 v74, v74, v75
	v_cndmask_b32_e32 v1, v220, v76, vcc
	v_lshlrev_b32_e32 v1, 2, v1
	ds_bpermute_b32 v75, v1, v74
	s_waitcnt lgkmcnt(0)
	v_add_f32_e32 v70, v74, v75
	v_fmamk_f32 v70, v70, 0x3a000000, v221
	v_mul_f32_e32 v71, 0x4f800000, v70
	v_cmp_gt_f32_e32 vcc, s56, v70
	s_nop 1
	v_cndmask_b32_e32 v124, v70, v71, vcc
	v_sqrt_f32_e32 v216, v124
	global_load_dwordx4 v[94:97], v[126:127], off offset:512
	global_load_dwordx4 v[70:73], v[126:127], off offset:3072
	global_load_dwordx4 v[74:77], v[126:127], off offset:3328
	global_load_dwordx4 v[78:81], v[126:127], off offset:3584
	v_add_u32_e32 v217, -1, v216
	v_fma_f32 v226, -v217, v216, v124
	v_cmp_ge_f32_e64 s[6:7], 0, v226
	v_add_u32_e32 v226, 1, v216
	s_nop 0
	v_cndmask_b32_e64 v217, v216, v217, s[6:7]
	v_fma_f32 v216, -v226, v216, v124
	v_cmp_lt_f32_e64 s[6:7], 0, v216
	s_nop 1
	v_cndmask_b32_e64 v216, v217, v226, s[6:7]
	v_mul_f32_e32 v217, 0x37800000, v216
	v_cndmask_b32_e32 v216, v216, v217, vcc
	v_cmp_class_f32_e32 vcc, v124, v222
	s_nop 1
	v_cndmask_b32_e32 v124, v216, v124, vcc
	v_div_scale_f32 v216, s[6:7], v124, v124, 1.0
	v_rcp_f32_e32 v217, v216
	s_lshl_b64 s[6:7], s[54:55], 12
	v_fma_f32 v226, -v216, v217, 1.0
	v_fmac_f32_e32 v217, v226, v217
	v_div_scale_f32 v226, vcc, 1.0, v124, 1.0
	v_mul_f32_e32 v227, v226, v217
	v_fma_f32 v228, -v216, v227, v226
	v_fmac_f32_e32 v227, v228, v217
	v_fma_f32 v216, -v216, v227, v226
	v_div_fmas_f32 v216, v216, v217, v227
	v_div_fixup_f32 v124, v216, v124, 1.0
	v_pk_mul_f32 v[118:119], v[118:119], v[124:125] op_sel_hi:[1,0]
	v_pk_mul_f32 v[120:121], v[120:121], v[124:125] op_sel_hi:[1,0]
	v_pk_mul_f32 v[114:115], v[114:115], v[124:125] op_sel_hi:[1,0]
	v_pk_mul_f32 v[116:117], v[116:117], v[124:125] op_sel_hi:[1,0]
	v_pk_mul_f32 v[120:121], v[8:9], v[120:121]
	v_pk_mul_f32 v[118:119], v[6:7], v[118:119]
	v_pk_mul_f32 v[116:117], v[4:5], v[116:117]
	v_pk_mul_f32 v[114:115], v[2:3], v[114:115]
	v_lshl_add_u64 v[216:217], v[130:131], 0, s[6:7]
	v_cvt_pk_bf16_f32 v226, v118, v119
	v_cvt_pk_bf16_f32 v227, v120, v121
	v_cvt_pk_bf16_f32 v228, v114, v115
	v_cvt_pk_bf16_f32 v229, v116, v117
	v_pk_mul_f32 v[110:111], v[110:111], v[124:125] op_sel_hi:[1,0]
	v_pk_mul_f32 v[112:113], v[112:113], v[124:125] op_sel_hi:[1,0]
	v_pk_mul_f32 v[106:107], v[106:107], v[124:125] op_sel_hi:[1,0]
	v_pk_mul_f32 v[108:109], v[108:109], v[124:125] op_sel_hi:[1,0]
	global_store_dwordx4 v[216:217], v[226:229], off
	v_pk_mul_f32 v[112:113], v[16:17], v[112:113]
	v_pk_mul_f32 v[110:111], v[14:15], v[110:111]
	v_add_u32_e32 v226, s26, v122
	v_pk_mul_f32 v[108:109], v[12:13], v[108:109]
	v_pk_mul_f32 v[106:107], v[10:11], v[106:107]
	ds_write_b128 v226, v[118:121]
	ds_write_b128 v226, v[114:117] offset:16
	v_cvt_pk_bf16_f32 v114, v110, v111
	v_cvt_pk_bf16_f32 v115, v112, v113
	v_cvt_pk_bf16_f32 v116, v106, v107
	v_cvt_pk_bf16_f32 v117, v108, v109
	global_store_dwordx4 v[216:217], v[114:117], off offset:1024
	ds_write_b128 v226, v[110:113] offset:2048
	ds_write_b128 v226, v[106:109] offset:2064
	s_waitcnt vmcnt(15)
	v_mov_b32_e32 v108, v55
	s_waitcnt vmcnt(14)
	v_mov_b32_e32 v109, v51
	v_mov_b32_e32 v106, v54
	v_mov_b32_e32 v107, v50
	v_pk_mul_f32 v[108:109], v[108:109], v[108:109]
	v_mov_b32_e32 v110, v57
	v_mov_b32_e32 v111, v53
	v_pk_fma_f32 v[106:107], v[106:107], v[106:107], v[108:109]
	v_mov_b32_e32 v108, v56
	v_mov_b32_e32 v109, v52
	v_pk_mul_f32 v[110:111], v[110:111], v[110:111]
	v_pk_mul_f32 v[90:91], v[90:91], v[124:125] op_sel_hi:[1,0]
	v_pk_fma_f32 v[108:109], v[108:109], v[108:109], v[110:111]
	s_waitcnt vmcnt(12)
	v_pk_mul_f32 v[110:111], v[46:47], v[46:47]
	v_pk_add_f32 v[106:107], v[106:107], v[108:109]
	v_pk_mul_f32 v[108:109], v[48:49], v[48:49]
	v_pk_add_f32 v[106:107], v[106:107], v[106:107] op_sel:[0,1] op_sel_hi:[1,0]
	v_pk_mov_b32 v[112:113], v[110:111], v[108:109] op_sel:[1,0]
	v_mov_b32_e32 v111, v109
	v_pk_add_f32 v[108:109], v[112:113], v[110:111]
	s_waitcnt vmcnt(11)
	v_mul_f32_e32 v110, v38, v38
	v_mul_f32_e32 v111, v39, v39
	v_pk_add_f32 v[108:109], v[108:109], v[108:109] op_sel:[0,1] op_sel_hi:[1,0]
	v_mov_b32_e32 v107, v110
	v_mov_b32_e32 v109, v111
	v_pk_add_f32 v[106:107], v[106:107], v[108:109]
	v_mul_f32_e32 v108, v43, v43
	v_mul_f32_e32 v110, v45, v45
	v_mul_f32_e32 v112, v40, v40
	v_mul_f32_e32 v113, v41, v41
	v_pk_fma_f32 v[108:109], v[42:43], v[42:43], v[108:109] op_sel_hi:[1,1,0]
	v_pk_fma_f32 v[110:111], v[44:45], v[44:45], v[110:111] op_sel_hi:[1,1,0]
	v_mov_b32_e32 v109, v112
	v_mov_b32_e32 v111, v113
	v_pk_add_f32 v[108:109], v[108:109], v[110:111]
	s_waitcnt vmcnt(10)
	v_pk_mul_f32 v[110:111], v[34:35], v[34:35]
	v_pk_add_f32 v[106:107], v[106:107], v[108:109]
	v_pk_mul_f32 v[108:109], v[36:37], v[36:37]
	v_pk_add_f32 v[106:107], v[106:107], v[106:107] op_sel:[0,1] op_sel_hi:[1,0]
	v_pk_mov_b32 v[112:113], v[110:111], v[108:109] op_sel:[1,0]
	v_mov_b32_e32 v111, v109
	v_pk_add_f32 v[108:109], v[112:113], v[110:111]
	s_waitcnt vmcnt(8)
	v_mul_f32_e32 v110, v98, v98
	v_mul_f32_e32 v111, v99, v99
	v_pk_add_f32 v[108:109], v[108:109], v[108:109] op_sel:[0,1] op_sel_hi:[1,0]
	v_mov_b32_e32 v107, v110
	v_mov_b32_e32 v109, v111
	v_pk_add_f32 v[106:107], v[106:107], v[108:109]
	v_mul_f32_e32 v108, v103, v103
	v_mul_f32_e32 v110, v105, v105
	v_mul_f32_e32 v112, v100, v100
	v_mul_f32_e32 v113, v101, v101
	v_pk_fma_f32 v[108:109], v[102:103], v[102:103], v[108:109] op_sel_hi:[1,1,0]
	v_pk_fma_f32 v[110:111], v[104:105], v[104:105], v[110:111] op_sel_hi:[1,1,0]
	v_mov_b32_e32 v109, v112
	v_mov_b32_e32 v111, v113
	v_pk_add_f32 v[108:109], v[108:109], v[110:111]
	v_pk_mul_f32 v[92:93], v[92:93], v[124:125] op_sel_hi:[1,0]
	v_pk_add_f32 v[106:107], v[106:107], v[108:109]
	v_pk_mul_f32 v[66:67], v[66:67], v[124:125] op_sel_hi:[1,0]
	v_add_f32_e32 v106, v106, v107
	s_nop 1
	v_mov_b32_dpp v107, v106 quad_perm:[1,0,3,2] row_mask:0xf bank_mask:0xf
	s_nop 1
	v_pk_mul_f32 v[68:69], v[68:69], v[124:125] op_sel_hi:[1,0]
	v_pk_mul_f32 v[92:93], v[20:21], v[92:93]
	v_pk_mul_f32 v[90:91], v[18:19], v[90:91]
	v_pk_mul_f32 v[68:69], v[28:29], v[68:69]
	s_waitcnt lgkmcnt(0)
	v_add_f32_e32 v107, v106, v107
	s_nop 1
	v_mov_b32_dpp v108, v107 quad_perm:[2,3,0,1] row_mask:0xf bank_mask:0xf
	s_nop 1
	v_pk_mul_f32 v[66:67], v[26:27], v[66:67]
	v_cvt_pk_bf16_f32 v106, v90, v91
	v_cvt_pk_bf16_f32 v109, v68, v69
	v_pk_mul_f32 v[62:63], v[62:63], v[124:125] op_sel_hi:[1,0]
	s_waitcnt lgkmcnt(0)
	v_add_f32_e32 v110, v107, v108
	s_nop 1
	v_mov_b32_dpp v111, v110 row_half_mirror row_mask:0xf bank_mask:0xf
	s_nop 1
	v_cvt_pk_bf16_f32 v107, v92, v93
	v_cvt_pk_bf16_f32 v108, v66, v67
	global_store_dwordx4 v[216:217], v[106:109], off offset:2048
	ds_write_b128 v226, v[90:93] offset:4096
	ds_write_b128 v226, v[66:69] offset:4112
	s_waitcnt lgkmcnt(2)
	v_add_f32_e32 v106, v110, v111
	s_nop 1
	v_mov_b32_dpp v107, v106 row_mirror row_mask:0xf bank_mask:0xf
	s_nop 1
	v_pk_mul_f32 v[64:65], v[64:65], v[124:125] op_sel_hi:[1,0]
	v_pk_mul_f32 v[58:59], v[58:59], v[124:125] op_sel_hi:[1,0]
	v_pk_mul_f32 v[60:61], v[60:61], v[124:125] op_sel_hi:[1,0]
	v_pk_mul_f32 v[64:65], v[24:25], v[64:65]
	s_waitcnt lgkmcnt(0)
	v_add_f32_e32 v66, v106, v107
	ds_bpermute_b32 v67, v232, v66
	v_pk_mul_f32 v[62:63], v[22:23], v[62:63]
	v_pk_mul_f32 v[60:61], v[32:33], v[60:61]
	v_pk_mul_f32 v[58:59], v[30:31], v[58:59]
	v_cvt_pk_bf16_f32 v69, v60, v61
	s_waitcnt lgkmcnt(0)
	v_add_f32_e32 v68, v66, v67
	ds_bpermute_b32 v1, v1, v68
	v_cvt_pk_bf16_f32 v66, v62, v63
	v_cvt_pk_bf16_f32 v67, v64, v65
	s_waitcnt lgkmcnt(0)
	v_add_f32_e32 v1, v68, v1
	v_fmamk_f32 v1, v1, 0x3a000000, v221
	v_mul_f32_e32 v68, 0x4f800000, v1
	v_cmp_gt_f32_e32 vcc, s56, v1
	s_nop 1
	v_cndmask_b32_e32 v1, v1, v68, vcc
	v_sqrt_f32_e32 v90, v1
	v_cvt_pk_bf16_f32 v68, v58, v59
	global_store_dwordx4 v[216:217], v[66:69], off offset:3072
	ds_write_b128 v226, v[62:65] offset:6144
	ds_write_b128 v226, v[58:61] offset:6160
	v_add_u32_e32 v66, -1, v90
	v_fma_f32 v67, -v66, v90, v1
	v_cmp_ge_f32_e64 s[6:7], 0, v67
	v_add_u32_e32 v67, 1, v90
	v_fma_f32 v68, -v67, v90, v1
	v_cndmask_b32_e64 v66, v90, v66, s[6:7]
	v_cmp_lt_f32_e64 s[6:7], 0, v68
	s_nop 1
	v_cndmask_b32_e64 v66, v66, v67, s[6:7]
	v_mul_f32_e32 v67, 0x37800000, v66
	v_cndmask_b32_e32 v66, v66, v67, vcc
	v_cmp_class_f32_e32 vcc, v1, v222
	s_nop 1
	v_cndmask_b32_e32 v1, v66, v1, vcc
	v_div_scale_f32 v66, s[6:7], v1, v1, 1.0
	v_rcp_f32_e32 v67, v66
	s_lshl_b64 s[6:7], s[58:59], 12
	v_lshl_add_u64 v[64:65], v[130:131], 0, s[6:7]
	v_fma_f32 v58, -v66, v67, 1.0
	v_fmac_f32_e32 v67, v58, v67
	v_div_scale_f32 v58, vcc, 1.0, v1, 1.0
	v_mul_f32_e32 v59, v58, v67
	v_fma_f32 v60, -v66, v59, v58
	v_fmac_f32_e32 v59, v60, v67
	v_fma_f32 v58, -v66, v59, v58
	v_div_fmas_f32 v58, v58, v67, v59
	v_div_fixup_f32 v62, v58, v1, 1.0
	v_pk_mul_f32 v[54:55], v[54:55], v[62:63] op_sel_hi:[1,0]
	v_pk_mul_f32 v[56:57], v[56:57], v[62:63] op_sel_hi:[1,0]
	v_pk_mul_f32 v[50:51], v[50:51], v[62:63] op_sel_hi:[1,0]
	v_pk_mul_f32 v[52:53], v[52:53], v[62:63] op_sel_hi:[1,0]
	v_pk_mul_f32 v[56:57], v[8:9], v[56:57]
	v_pk_mul_f32 v[54:55], v[6:7], v[54:55]
	v_pk_mul_f32 v[52:53], v[4:5], v[52:53]
	v_pk_mul_f32 v[50:51], v[2:3], v[50:51]
	v_pk_mul_f32 v[46:47], v[46:47], v[62:63] op_sel_hi:[1,0]
	v_pk_mul_f32 v[48:49], v[48:49], v[62:63] op_sel_hi:[1,0]
	v_pk_mul_f32 v[42:43], v[42:43], v[62:63] op_sel_hi:[1,0]
	v_pk_mul_f32 v[44:45], v[44:45], v[62:63] op_sel_hi:[1,0]
	v_cvt_pk_bf16_f32 v58, v54, v55
	v_cvt_pk_bf16_f32 v59, v56, v57
	v_cvt_pk_bf16_f32 v60, v50, v51
	v_cvt_pk_bf16_f32 v61, v52, v53
	v_add_u32_e32 v1, s33, v122
	v_pk_mul_f32 v[48:49], v[16:17], v[48:49]
	v_pk_mul_f32 v[46:47], v[14:15], v[46:47]
	v_pk_mul_f32 v[44:45], v[12:13], v[44:45]
	v_pk_mul_f32 v[42:43], v[10:11], v[42:43]
	v_pk_mul_f32 v[38:39], v[38:39], v[62:63] op_sel_hi:[1,0]
	v_pk_mul_f32 v[40:41], v[40:41], v[62:63] op_sel_hi:[1,0]
	v_pk_mul_f32 v[34:35], v[34:35], v[62:63] op_sel_hi:[1,0]
	v_pk_mul_f32 v[36:37], v[36:37], v[62:63] op_sel_hi:[1,0]
	global_store_dwordx4 v[64:65], v[58:61], off
	ds_write_b128 v1, v[54:57]
	ds_write_b128 v1, v[50:53] offset:16
	v_cvt_pk_bf16_f32 v50, v46, v47
	v_cvt_pk_bf16_f32 v51, v48, v49
	v_cvt_pk_bf16_f32 v52, v42, v43
	v_cvt_pk_bf16_f32 v53, v44, v45
	v_pk_mul_f32 v[40:41], v[20:21], v[40:41]
	v_pk_mul_f32 v[38:39], v[18:19], v[38:39]
	v_pk_mul_f32 v[36:37], v[28:29], v[36:37]
	v_pk_mul_f32 v[34:35], v[26:27], v[34:35]
	global_store_dwordx4 v[64:65], v[50:53], off offset:1024
	ds_write_b128 v1, v[46:49] offset:2048
	ds_write_b128 v1, v[42:45] offset:2064
	v_cvt_pk_bf16_f32 v42, v38, v39
	v_cvt_pk_bf16_f32 v43, v40, v41
	v_cvt_pk_bf16_f32 v44, v34, v35
	v_cvt_pk_bf16_f32 v45, v36, v37
	global_store_dwordx4 v[64:65], v[42:45], off offset:2048
	ds_write_b128 v1, v[38:41] offset:4096
	ds_write_b128 v1, v[34:37] offset:4112
	v_pk_mul_f32 v[34:35], v[102:103], v[62:63] op_sel_hi:[1,0]
	v_pk_mul_f32 v[36:37], v[104:105], v[62:63] op_sel_hi:[1,0]
	v_pk_mul_f32 v[38:39], v[98:99], v[62:63] op_sel_hi:[1,0]
	v_pk_mul_f32 v[40:41], v[100:101], v[62:63] op_sel_hi:[1,0]
	v_pk_mul_f32 v[36:37], v[24:25], v[36:37]
	v_pk_mul_f32 v[34:35], v[22:23], v[34:35]
	v_pk_mul_f32 v[40:41], v[32:33], v[40:41]
	v_pk_mul_f32 v[38:39], v[30:31], v[38:39]
	v_cvt_pk_bf16_f32 v42, v34, v35
	v_cvt_pk_bf16_f32 v43, v36, v37
	v_cvt_pk_bf16_f32 v44, v38, v39
	v_cvt_pk_bf16_f32 v45, v40, v41
	global_store_dwordx4 v[64:65], v[42:45], off offset:3072
	ds_write_b128 v1, v[34:37] offset:6144
	ds_write_b128 v1, v[38:41] offset:6160
	s_waitcnt lgkmcnt(0)
	s_barrier
	v_add_u32_e32 v216, 0x1800, v255
	global_load_dwordx4 v[132:135], v216, s[94:95]
	v_add_u32_e32 v216, 0x1900, v255
	global_load_dwordx4 v[136:139], v216, s[94:95]
	v_add_u32_e32 v216, 0x1a00, v255
	global_load_dwordx4 v[140:143], v216, s[94:95]
	v_add_u32_e32 v216, 0x2400, v255
	global_load_dwordx4 v[144:147], v216, s[94:95]
	v_add_u32_e32 v216, 0x2500, v255
	global_load_dwordx4 v[148:151], v216, s[94:95]
	v_add_u32_e32 v216, 0x2600, v255
	global_load_dwordx4 v[152:155], v216, s[94:95]
	v_add_u32_e32 v216, 0x3000, v255
	global_load_dwordx4 v[156:159], v216, s[94:95]
	v_add_u32_e32 v216, 0x3100, v255
	global_load_dwordx4 v[160:163], v216, s[94:95]
	v_add_u32_e32 v216, 0x3200, v255
	global_load_dwordx4 v[164:167], v216, s[94:95]
	v_add_u32_e32 v216, 0x3c00, v255
	global_load_dwordx4 v[168:171], v216, s[94:95]
	v_add_u32_e32 v216, 0x3d00, v255
	global_load_dwordx4 v[172:175], v216, s[94:95]
	v_add_u32_e32 v216, 0x3e00, v255
	global_load_dwordx4 v[176:179], v216, s[94:95]
	v_add_u32_e32 v216, 0x4800, v255
	global_load_dwordx4 v[180:183], v216, s[94:95]
	v_add_u32_e32 v216, 0x4900, v255
	global_load_dwordx4 v[184:187], v216, s[94:95]
	v_add_u32_e32 v216, 0x4a00, v255
	global_load_dwordx4 v[188:191], v216, s[94:95]
	v_add_u32_e32 v216, 0x5400, v255
	global_load_dwordx4 v[192:195], v216, s[94:95]
	v_add_u32_e32 v216, 0x5500, v255
	global_load_dwordx4 v[226:229], v216, s[94:95]
	v_add_u32_e32 v216, 0x5600, v255
	global_load_dwordx4 v[230:233], v216, s[94:95]
	ds_read_b128 v[234:237], v123
	ds_read_b128 v[238:241], v123 offset:64
	s_waitcnt vmcnt(31) lgkmcnt(1)
	v_mfma_f32_16x16x4_f32 v[242:245], v234, v82, 0
	s_waitcnt vmcnt(30)
	v_mfma_f32_16x16x4_f32 v[246:249], v234, v86, 0
	s_waitcnt vmcnt(29)
	v_mfma_f32_16x16x4_f32 v[250:253], v234, v94, 0
	v_mfma_f32_16x16x4_f32 v[242:245], v235, v83, v[242:245]
	v_mfma_f32_16x16x4_f32 v[246:249], v235, v87, v[246:249]
	v_mfma_f32_16x16x4_f32 v[250:253], v235, v95, v[250:253]
	v_mfma_f32_16x16x4_f32 v[242:245], v236, v84, v[242:245]
	v_mfma_f32_16x16x4_f32 v[246:249], v236, v88, v[246:249]
	v_mfma_f32_16x16x4_f32 v[250:253], v236, v96, v[250:253]
	v_mfma_f32_16x16x4_f32 v[82:85], v237, v85, v[242:245]
	v_mfma_f32_16x16x4_f32 v[86:89], v237, v89, v[246:249]
	v_mfma_f32_16x16x4_f32 v[94:97], v237, v97, v[250:253]
	s_waitcnt vmcnt(28) lgkmcnt(0)
	v_mfma_f32_16x16x4_f32 v[82:85], v238, v70, v[82:85]
	s_waitcnt vmcnt(27)
	v_mfma_f32_16x16x4_f32 v[86:89], v238, v74, v[86:89]
	s_waitcnt vmcnt(26)
	v_mfma_f32_16x16x4_f32 v[94:97], v238, v78, v[94:97]
	v_mfma_f32_16x16x4_f32 v[82:85], v239, v71, v[82:85]
	v_mfma_f32_16x16x4_f32 v[86:89], v239, v75, v[86:89]
	v_mfma_f32_16x16x4_f32 v[94:97], v239, v79, v[94:97]
	v_mfma_f32_16x16x4_f32 v[82:85], v240, v72, v[82:85]
	v_mfma_f32_16x16x4_f32 v[86:89], v240, v76, v[86:89]
	v_mfma_f32_16x16x4_f32 v[94:97], v240, v80, v[94:97]
	v_mfma_f32_16x16x4_f32 v[70:73], v241, v73, v[82:85]
	v_mfma_f32_16x16x4_f32 v[74:77], v241, v77, v[86:89]
	s_nop 5
	ds_read_b128 v[82:85], v123 offset:128
	ds_read_b128 v[86:89], v123 offset:192
	v_mfma_f32_16x16x4_f32 v[78:81], v241, v81, v[94:97]
	s_waitcnt vmcnt(17) lgkmcnt(1)
	v_mfma_f32_16x16x4_f32 v[70:73], v82, v132, v[70:73]
	s_waitcnt vmcnt(16)
	v_mfma_f32_16x16x4_f32 v[74:77], v82, v136, v[74:77]
	s_waitcnt vmcnt(15)
	v_mfma_f32_16x16x4_f32 v[78:81], v82, v140, v[78:81]
	v_mfma_f32_16x16x4_f32 v[70:73], v83, v133, v[70:73]
	v_mfma_f32_16x16x4_f32 v[74:77], v83, v137, v[74:77]
	v_mfma_f32_16x16x4_f32 v[78:81], v83, v141, v[78:81]
	v_mfma_f32_16x16x4_f32 v[70:73], v84, v134, v[70:73]
	v_mfma_f32_16x16x4_f32 v[74:77], v84, v138, v[74:77]
	v_mfma_f32_16x16x4_f32 v[78:81], v84, v142, v[78:81]
	v_mfma_f32_16x16x4_f32 v[132:135], v85, v135, v[70:73]
	v_mfma_f32_16x16x4_f32 v[136:139], v85, v139, v[74:77]
	v_mfma_f32_16x16x4_f32 v[140:143], v85, v143, v[78:81]
	s_waitcnt vmcnt(12) lgkmcnt(0)
	v_mfma_f32_16x16x4_f32 v[140:143], v86, v152, v[140:143]
	v_mfma_f32_16x16x4_f32 v[132:135], v86, v144, v[132:135]
	v_mfma_f32_16x16x4_f32 v[136:139], v86, v148, v[136:139]
	v_mfma_f32_16x16x4_f32 v[140:143], v87, v153, v[140:143]
	v_mfma_f32_16x16x4_f32 v[132:135], v87, v145, v[132:135]
	v_mfma_f32_16x16x4_f32 v[136:139], v87, v149, v[136:139]
	v_mfma_f32_16x16x4_f32 v[140:143], v88, v154, v[140:143]
	v_mfma_f32_16x16x4_f32 v[132:135], v88, v146, v[132:135]
	v_mfma_f32_16x16x4_f32 v[136:139], v88, v150, v[136:139]
	v_mfma_f32_16x16x4_f32 v[132:135], v89, v147, v[132:135]
	v_add_u32_e32 v216, 0x6000, v255
	global_load_dwordx4 v[144:147], v216, s[94:95]
	v_add_u32_e32 v216, 0x6100, v255
	global_load_dwordx4 v[70:73], v216, s[94:95]
	v_add_u32_e32 v216, 0x6200, v255
	global_load_dwordx4 v[74:77], v216, s[94:95]
	v_add_u32_e32 v216, 0x6c00, v255
	global_load_dwordx4 v[78:81], v216, s[94:95]
	v_mfma_f32_16x16x4_f32 v[136:139], v89, v151, v[136:139]
	v_add_u32_e32 v216, 0x6d00, v255
	global_load_dwordx4 v[148:151], v216, s[94:95]
	v_add_u32_e32 v216, 0x6e00, v255
	global_load_dwordx4 v[82:85], v216, s[94:95]
	v_add_u32_e32 v216, 0x7800, v255
	global_load_dwordx4 v[94:97], v216, s[94:95]
	v_add_u32_e32 v216, 0x7900, v255
	global_load_dwordx4 v[234:237], v216, s[94:95]
	v_add_u32_e32 v216, 0x7a00, v255
	global_load_dwordx4 v[238:241], v216, s[94:95]
	v_add_u32_e32 v216, 0x8400, v255
	global_load_dwordx4 v[242:245], v216, s[94:95]
	v_add_u32_e32 v216, 0x8500, v255
	global_load_dwordx4 v[246:249], v216, s[94:95]
	v_add_u32_e32 v216, 0x8600, v255
	global_load_dwordx4 v[250:253], v216, s[94:95]
	v_mfma_f32_16x16x4_f32 v[140:143], v89, v155, v[140:143]
	ds_read_b128 v[152:155], v123 offset:256
	ds_read_b128 v[86:89], v123 offset:320
	s_waitcnt vmcnt(23) lgkmcnt(1)
	v_mfma_f32_16x16x4_f32 v[132:135], v152, v156, v[132:135]
	s_waitcnt vmcnt(22)
	v_mfma_f32_16x16x4_f32 v[136:139], v152, v160, v[136:139]
	s_waitcnt vmcnt(21)
	v_mfma_f32_16x16x4_f32 v[140:143], v152, v164, v[140:143]
	v_mfma_f32_16x16x4_f32 v[132:135], v153, v157, v[132:135]
	v_mfma_f32_16x16x4_f32 v[136:139], v153, v161, v[136:139]
	v_mfma_f32_16x16x4_f32 v[140:143], v153, v165, v[140:143]
	v_mfma_f32_16x16x4_f32 v[132:135], v154, v158, v[132:135]
	v_mfma_f32_16x16x4_f32 v[136:139], v154, v162, v[136:139]
	v_mfma_f32_16x16x4_f32 v[140:143], v154, v166, v[140:143]
	v_mfma_f32_16x16x4_f32 v[132:135], v155, v159, v[132:135]
	v_mfma_f32_16x16x4_f32 v[136:139], v155, v163, v[136:139]
	v_mfma_f32_16x16x4_f32 v[140:143], v155, v167, v[140:143]
	ds_read_b128 v[152:155], v123 offset:384
	ds_read_b128 v[156:159], v123 offset:448
	s_waitcnt vmcnt(20) lgkmcnt(2)
	v_mfma_f32_16x16x4_f32 v[132:135], v86, v168, v[132:135]
	s_waitcnt vmcnt(19)
	v_mfma_f32_16x16x4_f32 v[136:139], v86, v172, v[136:139]
	s_waitcnt vmcnt(18)
	v_mfma_f32_16x16x4_f32 v[140:143], v86, v176, v[140:143]
	v_mfma_f32_16x16x4_f32 v[132:135], v87, v169, v[132:135]
	v_mfma_f32_16x16x4_f32 v[136:139], v87, v173, v[136:139]
	v_mfma_f32_16x16x4_f32 v[140:143], v87, v177, v[140:143]
	v_mfma_f32_16x16x4_f32 v[132:135], v88, v170, v[132:135]
	v_mfma_f32_16x16x4_f32 v[136:139], v88, v174, v[136:139]
	v_mfma_f32_16x16x4_f32 v[140:143], v88, v178, v[140:143]
	v_mfma_f32_16x16x4_f32 v[132:135], v89, v171, v[132:135]
	v_mfma_f32_16x16x4_f32 v[136:139], v89, v175, v[136:139]
	v_mfma_f32_16x16x4_f32 v[140:143], v89, v179, v[140:143]
	s_waitcnt vmcnt(17) lgkmcnt(1)
	v_mfma_f32_16x16x4_f32 v[132:135], v152, v180, v[132:135]
	s_waitcnt vmcnt(16)
	v_mfma_f32_16x16x4_f32 v[136:139], v152, v184, v[136:139]
	s_waitcnt vmcnt(15)
	v_mfma_f32_16x16x4_f32 v[140:143], v152, v188, v[140:143]
	v_mfma_f32_16x16x4_f32 v[132:135], v153, v181, v[132:135]
	v_mfma_f32_16x16x4_f32 v[136:139], v153, v185, v[136:139]
	v_mfma_f32_16x16x4_f32 v[140:143], v153, v189, v[140:143]
	v_mfma_f32_16x16x4_f32 v[132:135], v154, v182, v[132:135]
	v_mfma_f32_16x16x4_f32 v[136:139], v154, v186, v[136:139]
	v_mfma_f32_16x16x4_f32 v[140:143], v154, v190, v[140:143]
	v_mfma_f32_16x16x4_f32 v[132:135], v155, v183, v[132:135]
	v_mfma_f32_16x16x4_f32 v[136:139], v155, v187, v[136:139]
	v_mfma_f32_16x16x4_f32 v[140:143], v155, v191, v[140:143]
	v_add_u32_e32 v216, 0x9000, v255
	global_load_dwordx4 v[152:155], v216, s[94:95]
	v_add_u32_e32 v216, 0x9100, v255
	global_load_dwordx4 v[160:163], v216, s[94:95]
	v_add_u32_e32 v216, 0x9200, v255
	global_load_dwordx4 v[164:167], v216, s[94:95]
	v_add_u32_e32 v216, 0x9c00, v255
	global_load_dwordx4 v[86:89], v216, s[94:95]
	s_waitcnt vmcnt(16) lgkmcnt(0)
	v_mfma_f32_16x16x4_f32 v[140:143], v156, v230, v[140:143]
	v_mfma_f32_16x16x4_f32 v[132:135], v156, v192, v[132:135]
	v_mfma_f32_16x16x4_f32 v[136:139], v156, v226, v[136:139]
	v_mfma_f32_16x16x4_f32 v[140:143], v157, v231, v[140:143]
	v_mfma_f32_16x16x4_f32 v[132:135], v157, v193, v[132:135]
	v_mfma_f32_16x16x4_f32 v[136:139], v157, v227, v[136:139]
	v_mfma_f32_16x16x4_f32 v[140:143], v158, v232, v[140:143]
	v_mfma_f32_16x16x4_f32 v[132:135], v158, v194, v[132:135]
	v_mfma_f32_16x16x4_f32 v[136:139], v158, v228, v[136:139]
	v_mfma_f32_16x16x4_f32 v[132:135], v159, v195, v[132:135]
	v_mfma_f32_16x16x4_f32 v[136:139], v159, v229, v[136:139]
	v_add_u32_e32 v216, 0x9d00, v255
	global_load_dwordx4 v[168:171], v216, s[94:95]
	v_add_u32_e32 v216, 0x9e00, v255
	global_load_dwordx4 v[172:175], v216, s[94:95]
	v_add_u32_e32 v216, 0xa800, v255
	global_load_dwordx4 v[176:179], v216, s[94:95]
	v_add_u32_e32 v216, 0xa900, v255
	global_load_dwordx4 v[180:183], v216, s[94:95]
	v_add_u32_e32 v216, 0xaa00, v255
	global_load_dwordx4 v[184:187], v216, s[94:95]
	v_add_u32_e32 v216, 0xb400, v255
	global_load_dwordx4 v[188:191], v216, s[94:95]
	v_add_u32_e32 v216, 0xb500, v255
	global_load_dwordx4 v[192:195], v216, s[94:95]
	v_add_u32_e32 v216, 0xb600, v255
	global_load_dwordx4 v[226:229], v216, s[94:95]
	s_add_i32 s82, s68, 1
	s_min_u32 s82, s82, 3
	s_lshl_b32 s82, s82, 4
	s_add_i32 s82, s67, s82
	s_ashr_i32 s83, s82, 31
	s_lshl_b64 s[82:83], s[82:83], 13
	v_lshl_add_u64 v[98:99], v[128:129], 0, s[82:83]
	s_add_u32 s82, s82, 0x1000
	s_addc_u32 s83, s83, 0
	global_load_dwordx4 v[118:121], v[98:99], off
	global_load_dwordx4 v[114:117], v[98:99], off offset:16
	global_load_dwordx4 v[110:113], v[98:99], off offset:2048
	global_load_dwordx4 v[106:109], v[98:99], off offset:2064
	v_lshl_add_u64 v[100:101], v[128:129], 0, s[82:83]
	s_add_u32 s82, s82, 0x1000
	s_addc_u32 s83, s83, 0
	global_load_dwordx4 v[58:61], v[100:101], off offset:2064
	global_load_dwordx4 v[90:93], v[100:101], off
	global_load_dwordx4 v[66:69], v[100:101], off offset:16
	global_load_dwordx4 v[62:65], v[100:101], off offset:2048
	v_lshl_add_u64 v[98:99], v[128:129], 0, s[82:83]
	s_nop 0
	global_load_dwordx4 v[54:57], v[98:99], off
	global_load_dwordx4 v[50:53], v[98:99], off offset:16
	global_load_dwordx4 v[196:199], v[98:99], off offset:2064
	global_load_dwordx4 v[200:203], v[98:99], off offset:2048
	s_add_u32 s82, s82, 0x1000
	s_addc_u32 s83, s83, 0
	v_lshl_add_u64 v[100:101], v[128:129], 0, s[82:83]
	s_nop 0
	global_load_dwordx4 v[204:207], v[100:101], off
	global_load_dwordx4 v[208:211], v[100:101], off offset:16
	global_load_dwordx4 v[102:105], v[100:101], off offset:2048
	global_load_dwordx4 v[212:215], v[100:101], off offset:2064
	v_mfma_f32_16x16x4_f32 v[140:143], v159, v233, v[140:143]
	ds_read_b128 v[156:159], v123 offset:512
	ds_read_b128 v[230:233], v123 offset:576
	s_waitcnt vmcnt(39) lgkmcnt(1)
	v_mfma_f32_16x16x4_f32 v[132:135], v156, v144, v[132:135]
	s_waitcnt vmcnt(38)
	v_mfma_f32_16x16x4_f32 v[136:139], v156, v70, v[136:139]
	s_waitcnt vmcnt(37)
	v_mfma_f32_16x16x4_f32 v[140:143], v156, v74, v[140:143]
	v_mfma_f32_16x16x4_f32 v[132:135], v157, v145, v[132:135]
	v_mfma_f32_16x16x4_f32 v[136:139], v157, v71, v[136:139]
	v_mfma_f32_16x16x4_f32 v[140:143], v157, v75, v[140:143]
	v_mfma_f32_16x16x4_f32 v[132:135], v158, v146, v[132:135]
	v_mfma_f32_16x16x4_f32 v[136:139], v158, v72, v[136:139]
	v_mfma_f32_16x16x4_f32 v[140:143], v158, v76, v[140:143]
	v_mfma_f32_16x16x4_f32 v[132:135], v159, v147, v[132:135]
	v_mfma_f32_16x16x4_f32 v[136:139], v159, v73, v[136:139]
	v_mfma_f32_16x16x4_f32 v[140:143], v159, v77, v[140:143]
	s_waitcnt vmcnt(36) lgkmcnt(0)
	v_mfma_f32_16x16x4_f32 v[132:135], v230, v78, v[132:135]
	s_waitcnt vmcnt(35)
	v_mfma_f32_16x16x4_f32 v[136:139], v230, v148, v[136:139]
	s_waitcnt vmcnt(34)
	v_mfma_f32_16x16x4_f32 v[140:143], v230, v82, v[140:143]
	v_mfma_f32_16x16x4_f32 v[132:135], v231, v79, v[132:135]
	v_mfma_f32_16x16x4_f32 v[136:139], v231, v149, v[136:139]
	v_mfma_f32_16x16x4_f32 v[140:143], v231, v83, v[140:143]
	v_mfma_f32_16x16x4_f32 v[132:135], v232, v80, v[132:135]
	v_mfma_f32_16x16x4_f32 v[136:139], v232, v150, v[136:139]
	v_mfma_f32_16x16x4_f32 v[140:143], v232, v84, v[140:143]
	v_mfma_f32_16x16x4_f32 v[132:135], v233, v81, v[132:135]
	v_mfma_f32_16x16x4_f32 v[136:139], v233, v151, v[136:139]
	ds_read_b128 v[144:147], v123 offset:640
	ds_read_b128 v[148:151], v123 offset:704
	v_mfma_f32_16x16x4_f32 v[140:143], v233, v85, v[140:143]
	s_waitcnt vmcnt(33) lgkmcnt(1)
	v_mfma_f32_16x16x4_f32 v[132:135], v144, v94, v[132:135]
	s_waitcnt vmcnt(32)
	v_mfma_f32_16x16x4_f32 v[136:139], v144, v234, v[136:139]
	s_waitcnt vmcnt(31)
	v_mfma_f32_16x16x4_f32 v[140:143], v144, v238, v[140:143]
	v_mfma_f32_16x16x4_f32 v[132:135], v145, v95, v[132:135]
	v_mfma_f32_16x16x4_f32 v[136:139], v145, v235, v[136:139]
	v_mfma_f32_16x16x4_f32 v[140:143], v145, v239, v[140:143]
	v_mfma_f32_16x16x4_f32 v[132:135], v146, v96, v[132:135]
	v_mfma_f32_16x16x4_f32 v[136:139], v146, v236, v[136:139]
	v_mfma_f32_16x16x4_f32 v[140:143], v146, v240, v[140:143]
	v_mfma_f32_16x16x4_f32 v[132:135], v147, v97, v[132:135]
	v_mfma_f32_16x16x4_f32 v[136:139], v147, v237, v[136:139]
	v_mfma_f32_16x16x4_f32 v[140:143], v147, v241, v[140:143]
	s_waitcnt vmcnt(30) lgkmcnt(0)
	v_mfma_f32_16x16x4_f32 v[132:135], v148, v242, v[132:135]
	s_waitcnt vmcnt(29)
	v_mfma_f32_16x16x4_f32 v[136:139], v148, v246, v[136:139]
	s_waitcnt vmcnt(28)
	v_mfma_f32_16x16x4_f32 v[140:143], v148, v250, v[140:143]
	v_mfma_f32_16x16x4_f32 v[132:135], v149, v243, v[132:135]
	v_mfma_f32_16x16x4_f32 v[136:139], v149, v247, v[136:139]
	v_mfma_f32_16x16x4_f32 v[140:143], v149, v251, v[140:143]
	v_mfma_f32_16x16x4_f32 v[132:135], v150, v244, v[132:135]
	v_mfma_f32_16x16x4_f32 v[136:139], v150, v248, v[136:139]
	v_mfma_f32_16x16x4_f32 v[140:143], v150, v252, v[140:143]
	v_mfma_f32_16x16x4_f32 v[132:135], v151, v245, v[132:135]
	v_mfma_f32_16x16x4_f32 v[136:139], v151, v249, v[136:139]
	v_mfma_f32_16x16x4_f32 v[140:143], v151, v253, v[140:143]
	ds_read_b128 v[144:147], v123 offset:768
	ds_read_b128 v[148:151], v123 offset:832
	s_waitcnt vmcnt(27) lgkmcnt(1)
	v_mfma_f32_16x16x4_f32 v[132:135], v144, v152, v[132:135]
	s_waitcnt vmcnt(26)
	v_mfma_f32_16x16x4_f32 v[136:139], v144, v160, v[136:139]
	s_waitcnt vmcnt(25)
	v_mfma_f32_16x16x4_f32 v[140:143], v144, v164, v[140:143]
	v_mfma_f32_16x16x4_f32 v[132:135], v145, v153, v[132:135]
	v_mfma_f32_16x16x4_f32 v[136:139], v145, v161, v[136:139]
	v_mfma_f32_16x16x4_f32 v[140:143], v145, v165, v[140:143]
	v_mfma_f32_16x16x4_f32 v[132:135], v146, v154, v[132:135]
	v_mfma_f32_16x16x4_f32 v[136:139], v146, v162, v[136:139]
	v_mfma_f32_16x16x4_f32 v[140:143], v146, v166, v[140:143]
	v_mfma_f32_16x16x4_f32 v[132:135], v147, v155, v[132:135]
	v_mfma_f32_16x16x4_f32 v[136:139], v147, v163, v[136:139]
	v_mfma_f32_16x16x4_f32 v[140:143], v147, v167, v[140:143]
	s_waitcnt vmcnt(24) lgkmcnt(0)
	v_mfma_f32_16x16x4_f32 v[132:135], v148, v86, v[132:135]
	s_waitcnt vmcnt(23)
	v_mfma_f32_16x16x4_f32 v[136:139], v148, v168, v[136:139]
	s_waitcnt vmcnt(22)
	v_mfma_f32_16x16x4_f32 v[140:143], v148, v172, v[140:143]
	v_mfma_f32_16x16x4_f32 v[132:135], v149, v87, v[132:135]
	v_mfma_f32_16x16x4_f32 v[136:139], v149, v169, v[136:139]
	v_mfma_f32_16x16x4_f32 v[140:143], v149, v173, v[140:143]
	v_mfma_f32_16x16x4_f32 v[132:135], v150, v88, v[132:135]
	v_mfma_f32_16x16x4_f32 v[136:139], v150, v170, v[136:139]
	v_mfma_f32_16x16x4_f32 v[140:143], v150, v174, v[140:143]
	v_mfma_f32_16x16x4_f32 v[132:135], v151, v89, v[132:135]
	v_mfma_f32_16x16x4_f32 v[136:139], v151, v171, v[136:139]
	v_mfma_f32_16x16x4_f32 v[140:143], v151, v175, v[140:143]
	ds_read_b128 v[144:147], v123 offset:896
	ds_read_b128 v[148:151], v123 offset:960
	s_waitcnt vmcnt(21) lgkmcnt(1)
	v_mfma_f32_16x16x4_f32 v[132:135], v144, v176, v[132:135]
	s_waitcnt vmcnt(20)
	v_mfma_f32_16x16x4_f32 v[136:139], v144, v180, v[136:139]
	s_waitcnt vmcnt(19)
	v_mfma_f32_16x16x4_f32 v[140:143], v144, v184, v[140:143]
	v_mfma_f32_16x16x4_f32 v[132:135], v145, v177, v[132:135]
	v_mfma_f32_16x16x4_f32 v[136:139], v145, v181, v[136:139]
	v_mfma_f32_16x16x4_f32 v[140:143], v145, v185, v[140:143]
	v_mfma_f32_16x16x4_f32 v[132:135], v146, v178, v[132:135]
	v_mfma_f32_16x16x4_f32 v[136:139], v146, v182, v[136:139]
	v_mfma_f32_16x16x4_f32 v[140:143], v146, v186, v[140:143]
	v_mfma_f32_16x16x4_f32 v[132:135], v147, v179, v[132:135]
	v_mfma_f32_16x16x4_f32 v[136:139], v147, v183, v[136:139]
	v_mfma_f32_16x16x4_f32 v[140:143], v147, v187, v[140:143]
	s_waitcnt vmcnt(18) lgkmcnt(0)
	v_mfma_f32_16x16x4_f32 v[132:135], v148, v188, v[132:135]
	s_waitcnt vmcnt(17)
	v_mfma_f32_16x16x4_f32 v[136:139], v148, v192, v[136:139]
	s_waitcnt vmcnt(16)
	v_mfma_f32_16x16x4_f32 v[140:143], v148, v226, v[140:143]
	v_mfma_f32_16x16x4_f32 v[132:135], v149, v189, v[132:135]
	v_mfma_f32_16x16x4_f32 v[136:139], v149, v193, v[136:139]
	v_mfma_f32_16x16x4_f32 v[140:143], v149, v227, v[140:143]
	v_mfma_f32_16x16x4_f32 v[132:135], v150, v190, v[132:135]
	v_mfma_f32_16x16x4_f32 v[136:139], v150, v194, v[136:139]
	v_mfma_f32_16x16x4_f32 v[140:143], v150, v228, v[140:143]
	v_mfma_f32_16x16x4_f32 v[132:135], v151, v191, v[132:135]
	v_mfma_f32_16x16x4_f32 v[136:139], v151, v195, v[136:139]
	v_mfma_f32_16x16x4_f32 v[140:143], v151, v229, v[140:143]
	s_nop 8
	ds_write2_b32 v223, v132, v136 offset1:16
	ds_write2_b32 v223, v140, v133 offset0:32 offset1:48
	ds_write2_b32 v223, v137, v141 offset0:64 offset1:80
	ds_write2_b32 v223, v134, v138 offset0:96 offset1:112
	ds_write2_b32 v223, v142, v135 offset0:128 offset1:144
	ds_write2_b32 v223, v139, v143 offset0:160 offset1:176
	s_waitcnt lgkmcnt(0)
	s_barrier
	s_and_saveexec_b64 s[6:7], s[4:5]
	s_cbranch_execz .LBB0_595
	s_mov_b64 s[8:9], 0
	v_mov_b32_e32 v34, v0

.LBB0_975:
	s_ashr_i32 s13, s12, 31
	s_lshl_b64 s[0:1], s[12:13], 2
	s_add_u32 s16, s27, s0
	s_addc_u32 s17, s92, s1
	global_load_dwordx4 v[2:5], v[38:39], off offset:-4080
	global_load_dwordx4 v[6:9], v[38:39], off offset:-4096
	global_load_dwordx4 v[10:13], v[38:39], off offset:-2032
	global_load_dwordx4 v[14:17], v[38:39], off offset:-2048
	global_load_dwordx4 v[18:21], v[38:39], off offset:16
	global_load_dwordx4 v[22:25], v[38:39], off
	global_load_dwordx4 v[26:29], v[38:39], off offset:2064
	global_load_dwordx4 v[30:33], v[38:39], off offset:2048
	global_load_dwordx2 v[50:51], v35, s[16:17]
	s_add_i32 s18, s12, 1
	s_ashr_i32 s19, s18, 31
	s_add_u32 s0, s84, s0
	s_addc_u32 s1, s85, s1
	global_load_dword v34, v35, s[0:1]
	s_lshl_b64 s[16:17], s[18:19], 2
	s_add_u32 s0, s84, s16
	s_addc_u32 s1, s85, s17
	global_load_dword v58, v35, s[0:1]
	s_add_i32 s6, s6, s8
	s_add_i32 s12, s12, s2
	s_cmpk_lt_i32 s6, 0x4000
	s_waitcnt vmcnt(0)
	v_ashrrev_i32_e32 v53, 31, v50
	v_mov_b32_e32 v52, v50
	v_ashrrev_i32_e32 v55, 31, v51
	v_mov_b32_e32 v54, v51
	v_lshlrev_b64 v[50:51], 12, v[52:53]
	v_lshlrev_b64 v[52:53], 12, v[54:55]
	v_lshl_add_u64 v[60:61], v[36:37], 0, v[50:51]
	v_lshl_add_u64 v[62:63], v[36:37], 0, v[52:53]
	global_load_dwordx4 v[50:53], v[60:61], off
	global_load_dwordx4 v[54:57], v[62:63], off
	s_waitcnt vmcnt(0)
	v_lshlrev_b32_e32 v64, 16, v50
	v_lshlrev_b32_e32 v66, 16, v54
	v_and_b32_e32 v67, 0xffff0000, v54
	v_lshlrev_b32_e32 v54, 16, v55
	v_and_b32_e32 v55, 0xffff0000, v55
	v_and_b32_e32 v65, 0xffff0000, v50
	v_lshlrev_b32_e32 v50, 16, v51
	v_and_b32_e32 v51, 0xffff0000, v51
	v_lshlrev_b32_e32 v70, 16, v56
	v_and_b32_e32 v71, 0xffff0000, v56
	v_lshlrev_b32_e32 v56, 16, v57
	v_and_b32_e32 v57, 0xffff0000, v57
	v_pk_mul_f32 v[66:67], v[58:59], v[66:67] op_sel_hi:[0,1]
	v_pk_mul_f32 v[54:55], v[58:59], v[54:55] op_sel_hi:[0,1]
	v_lshlrev_b32_e32 v68, 16, v52
	v_and_b32_e32 v69, 0xffff0000, v52
	v_lshlrev_b32_e32 v52, 16, v53
	v_and_b32_e32 v53, 0xffff0000, v53
	v_pk_mul_f32 v[70:71], v[58:59], v[70:71] op_sel_hi:[0,1]
	v_pk_mul_f32 v[56:57], v[58:59], v[56:57] op_sel_hi:[0,1]
	v_pk_fma_f32 v[64:65], v[34:35], v[64:65], v[66:67] op_sel_hi:[0,1,1]
	v_pk_fma_f32 v[50:51], v[34:35], v[50:51], v[54:55] op_sel_hi:[0,1,1]
	v_pk_fma_f32 v[54:55], v[34:35], v[68:69], v[70:71] op_sel_hi:[0,1,1]
	v_pk_fma_f32 v[52:53], v[34:35], v[52:53], v[56:57] op_sel_hi:[0,1,1]
	v_pk_add_f32 v[6:7], v[6:7], v[64:65]
	v_pk_add_f32 v[8:9], v[8:9], v[50:51]
	v_pk_add_f32 v[2:3], v[2:3], v[54:55]
	v_pk_add_f32 v[4:5], v[4:5], v[52:53]
	global_store_dwordx4 v[38:39], v[6:9], off offset:-4096
	global_store_dwordx4 v[38:39], v[2:5], off offset:-4080
	global_load_dwordx4 v[50:53], v[60:61], off offset:1024
	global_load_dwordx4 v[54:57], v[62:63], off offset:1024
	v_mov_b32_e32 v66, v5
	v_mov_b32_e32 v67, v3
	v_mov_b32_e32 v70, v7
	v_mov_b32_e32 v71, v9
	v_mov_b32_e32 v64, v4
	v_mov_b32_e32 v65, v2
	v_mov_b32_e32 v68, v6
	v_mov_b32_e32 v69, v8
	v_pk_mul_f32 v[66:67], v[66:67], v[66:67]
	v_pk_mul_f32 v[70:71], v[70:71], v[70:71]
	v_pk_fma_f32 v[64:65], v[64:65], v[64:65], v[66:67]
	v_pk_fma_f32 v[66:67], v[68:69], v[68:69], v[70:71]
	s_waitcnt vmcnt(0)
	v_lshlrev_b32_e32 v70, 16, v52
	v_pk_add_f32 v[66:67], v[66:67], v[66:67] op_sel:[0,1] op_sel_hi:[1,0]
	v_lshlrev_b32_e32 v68, 16, v54
	v_pk_add_f32 v[66:67], v[64:65], v[66:67] op_sel:[1,0] op_sel_hi:[0,1]
	v_and_b32_e32 v69, 0xffff0000, v54
	v_lshlrev_b32_e32 v54, 16, v55
	v_and_b32_e32 v55, 0xffff0000, v55
	v_pk_add_f32 v[64:65], v[64:65], v[66:67]
	v_lshlrev_b32_e32 v66, 16, v50
	v_and_b32_e32 v67, 0xffff0000, v50
	v_lshlrev_b32_e32 v50, 16, v51
	v_and_b32_e32 v51, 0xffff0000, v51
	v_lshlrev_b32_e32 v72, 16, v56
	v_and_b32_e32 v73, 0xffff0000, v56
	v_lshlrev_b32_e32 v56, 16, v57
	v_and_b32_e32 v57, 0xffff0000, v57
	v_pk_mul_f32 v[68:69], v[58:59], v[68:69] op_sel_hi:[0,1]
	v_pk_mul_f32 v[54:55], v[58:59], v[54:55] op_sel_hi:[0,1]
	v_and_b32_e32 v71, 0xffff0000, v52
	v_lshlrev_b32_e32 v52, 16, v53
	v_and_b32_e32 v53, 0xffff0000, v53
	v_pk_mul_f32 v[72:73], v[58:59], v[72:73] op_sel_hi:[0,1]
	v_pk_mul_f32 v[56:57], v[58:59], v[56:57] op_sel_hi:[0,1]
	v_pk_fma_f32 v[66:67], v[34:35], v[66:67], v[68:69] op_sel_hi:[0,1,1]
	v_pk_fma_f32 v[50:51], v[34:35], v[50:51], v[54:55] op_sel_hi:[0,1,1]
	v_pk_fma_f32 v[54:55], v[34:35], v[70:71], v[72:73] op_sel_hi:[0,1,1]
	v_pk_fma_f32 v[52:53], v[34:35], v[52:53], v[56:57] op_sel_hi:[0,1,1]
	v_pk_add_f32 v[14:15], v[14:15], v[66:67]
	v_pk_add_f32 v[16:17], v[16:17], v[50:51]
	v_pk_add_f32 v[10:11], v[10:11], v[54:55]
	v_pk_add_f32 v[12:13], v[12:13], v[52:53]
	global_store_dwordx4 v[38:39], v[14:17], off offset:-2048
	global_store_dwordx4 v[38:39], v[10:13], off offset:-2032
	global_load_dwordx4 v[50:53], v[60:61], off offset:2048
	global_load_dwordx4 v[54:57], v[62:63], off offset:2048
	v_mov_b32_e32 v68, v13
	v_mov_b32_e32 v69, v11
	v_mov_b32_e32 v72, v15
	v_mov_b32_e32 v73, v17
	v_mov_b32_e32 v66, v12
	v_mov_b32_e32 v67, v10
	v_mov_b32_e32 v70, v14
	v_mov_b32_e32 v71, v16
	v_pk_mul_f32 v[68:69], v[68:69], v[68:69]
	v_pk_mul_f32 v[72:73], v[72:73], v[72:73]
	v_pk_fma_f32 v[66:67], v[66:67], v[66:67], v[68:69]
	v_pk_fma_f32 v[68:69], v[70:71], v[70:71], v[72:73]
	s_waitcnt vmcnt(0)
	v_lshlrev_b32_e32 v72, 16, v52
	v_pk_add_f32 v[68:69], v[68:69], v[68:69] op_sel:[0,1] op_sel_hi:[1,0]
	v_lshlrev_b32_e32 v70, 16, v54
	v_pk_add_f32 v[68:69], v[66:67], v[68:69] op_sel:[1,0] op_sel_hi:[0,1]
	v_and_b32_e32 v71, 0xffff0000, v54
	v_lshlrev_b32_e32 v54, 16, v55
	v_and_b32_e32 v55, 0xffff0000, v55
	v_pk_add_f32 v[66:67], v[66:67], v[68:69]
	v_lshlrev_b32_e32 v68, 16, v50
	v_and_b32_e32 v69, 0xffff0000, v50
	v_lshlrev_b32_e32 v50, 16, v51
	v_and_b32_e32 v51, 0xffff0000, v51
	v_lshlrev_b32_e32 v74, 16, v56
	v_and_b32_e32 v75, 0xffff0000, v56
	v_lshlrev_b32_e32 v56, 16, v57
	v_and_b32_e32 v57, 0xffff0000, v57
	v_pk_mul_f32 v[70:71], v[58:59], v[70:71] op_sel_hi:[0,1]
	v_pk_mul_f32 v[54:55], v[58:59], v[54:55] op_sel_hi:[0,1]
	v_and_b32_e32 v73, 0xffff0000, v52
	v_lshlrev_b32_e32 v52, 16, v53
	v_and_b32_e32 v53, 0xffff0000, v53
	v_pk_mul_f32 v[74:75], v[58:59], v[74:75] op_sel_hi:[0,1]
	v_pk_mul_f32 v[56:57], v[58:59], v[56:57] op_sel_hi:[0,1]
	v_pk_fma_f32 v[68:69], v[34:35], v[68:69], v[70:71] op_sel_hi:[0,1,1]
	v_pk_fma_f32 v[50:51], v[34:35], v[50:51], v[54:55] op_sel_hi:[0,1,1]
	v_pk_fma_f32 v[54:55], v[34:35], v[72:73], v[74:75] op_sel_hi:[0,1,1]
	v_pk_fma_f32 v[52:53], v[34:35], v[52:53], v[56:57] op_sel_hi:[0,1,1]
	v_pk_add_f32 v[22:23], v[22:23], v[68:69]
	v_pk_add_f32 v[24:25], v[24:25], v[50:51]
	v_pk_add_f32 v[18:19], v[18:19], v[54:55]
	v_pk_add_f32 v[20:21], v[20:21], v[52:53]
	global_store_dwordx4 v[38:39], v[22:25], off
	global_store_dwordx4 v[38:39], v[18:21], off offset:16
	global_load_dwordx4 v[50:53], v[60:61], off offset:3072
	global_load_dwordx4 v[54:57], v[62:63], off offset:3072
	v_mul_f32_e32 v70, v25, v25
	v_mul_f32_e32 v68, v23, v23
	v_pk_fma_f32 v[62:63], v[24:25], v[24:25], v[70:71] op_sel_hi:[1,1,0]
	v_pk_fma_f32 v[60:61], v[22:23], v[22:23], v[68:69] op_sel_hi:[1,1,0]
	v_mov_b32_e32 v78, v19
	v_mov_b32_e32 v74, v21
	v_mov_b32_e32 v76, v18
	v_mov_b32_e32 v72, v20
	s_waitcnt vmcnt(0)
	v_lshlrev_b32_e32 v68, 16, v50
	v_lshlrev_b32_e32 v70, 16, v54
	v_and_b32_e32 v71, 0xffff0000, v54
	v_lshlrev_b32_e32 v54, 16, v55
	v_and_b32_e32 v55, 0xffff0000, v55
	v_and_b32_e32 v69, 0xffff0000, v50
	v_lshlrev_b32_e32 v50, 16, v51
	v_and_b32_e32 v51, 0xffff0000, v51
	v_lshlrev_b32_e32 v82, 16, v56
	v_and_b32_e32 v83, 0xffff0000, v56
	v_lshlrev_b32_e32 v56, 16, v57
	v_and_b32_e32 v57, 0xffff0000, v57
	v_pk_mul_f32 v[70:71], v[58:59], v[70:71] op_sel_hi:[0,1]
	v_pk_mul_f32 v[54:55], v[58:59], v[54:55] op_sel_hi:[0,1]
	v_lshlrev_b32_e32 v80, 16, v52
	v_and_b32_e32 v81, 0xffff0000, v52
	v_lshlrev_b32_e32 v52, 16, v53
	v_and_b32_e32 v53, 0xffff0000, v53
	v_pk_mul_f32 v[82:83], v[58:59], v[82:83] op_sel_hi:[0,1]
	v_pk_mul_f32 v[56:57], v[58:59], v[56:57] op_sel_hi:[0,1]
	v_pk_fma_f32 v[58:59], v[34:35], v[68:69], v[70:71] op_sel_hi:[0,1,1]
	v_pk_fma_f32 v[50:51], v[34:35], v[50:51], v[54:55] op_sel_hi:[0,1,1]
	v_pk_fma_f32 v[54:55], v[34:35], v[80:81], v[82:83] op_sel_hi:[0,1,1]
	v_pk_fma_f32 v[52:53], v[34:35], v[52:53], v[56:57] op_sel_hi:[0,1,1]
	v_pk_add_f32 v[30:31], v[30:31], v[58:59]
	v_pk_add_f32 v[32:33], v[32:33], v[50:51]
	v_pk_add_f32 v[26:27], v[26:27], v[54:55]
	v_pk_add_f32 v[28:29], v[28:29], v[52:53]
	v_pk_mul_f32 v[52:53], v[32:33], v[32:33]
	v_mov_b32_e32 v79, v31
	v_pk_mul_f32 v[50:51], v[28:29], v[28:29]
	v_mov_b32_e32 v75, v27
	v_mov_b32_e32 v77, v30
	v_pk_mul_f32 v[54:55], v[78:79], v[78:79]
	v_mov_b32_e32 v61, v52
	v_mov_b32_e32 v63, v53
	v_mov_b32_e32 v73, v26
	v_mov_b32_e32 v65, v50
	v_mov_b32_e32 v67, v51
	v_pk_mul_f32 v[50:51], v[74:75], v[74:75]
	v_pk_fma_f32 v[54:55], v[76:77], v[76:77], v[54:55]
	v_pk_add_f32 v[56:57], v[60:61], v[62:63]
	v_pk_fma_f32 v[50:51], v[72:73], v[72:73], v[50:51]
	v_pk_add_f32 v[54:55], v[54:55], v[56:57]
	v_pk_add_f32 v[52:53], v[64:65], v[66:67]
	v_pk_add_f32 v[50:51], v[50:51], v[54:55]
	global_store_dwordx4 v[38:39], v[30:33], off offset:2048
	global_store_dwordx4 v[38:39], v[26:29], off offset:2064
	v_pk_add_f32 v[50:51], v[52:53], v[50:51]
	v_lshl_add_u64 v[38:39], v[38:39], 0, s[10:11]
	v_add_f32_e32 v1, v50, v51
	s_nop 1
	v_mov_b32_dpp v34, v1 quad_perm:[1,0,3,2] row_mask:0xf bank_mask:0xf
	s_nop 1
	s_waitcnt lgkmcnt(0)
	v_add_f32_e32 v1, v1, v34
	s_nop 1
	v_mov_b32_dpp v34, v1 quad_perm:[2,3,0,1] row_mask:0xf bank_mask:0xf
	s_nop 1
	s_waitcnt lgkmcnt(0)
	v_add_f32_e32 v1, v1, v34
	s_nop 1
	v_mov_b32_dpp v34, v1 row_half_mirror row_mask:0xf bank_mask:0xf
	s_nop 1
	s_waitcnt lgkmcnt(0)
	v_add_f32_e32 v1, v1, v34
	s_nop 1
	v_mov_b32_dpp v34, v1 row_mirror row_mask:0xf bank_mask:0xf
	s_nop 1
	s_waitcnt lgkmcnt(0)
	v_add_f32_e32 v1, v1, v34
	ds_bpermute_b32 v34, v46, v1
	s_waitcnt lgkmcnt(0)
	v_add_f32_e32 v1, v1, v34
	ds_bpermute_b32 v34, v47, v1
	s_waitcnt lgkmcnt(0)
	v_add_f32_e32 v1, v1, v34
	v_fmamk_f32 v1, v1, 0x3a000000, v48
	v_mul_f32_e32 v34, 0x4f800000, v1
	v_cmp_gt_f32_e32 vcc, s3, v1
	s_nop 1
	v_cndmask_b32_e32 v1, v1, v34, vcc
	v_sqrt_f32_e32 v34, v1
	s_nop 0
	v_add_u32_e32 v50, -1, v34
	v_add_u32_e32 v51, 1, v34
	v_fma_f32 v52, -v50, v34, v1
	v_fma_f32 v53, -v51, v34, v1
	v_cmp_ge_f32_e64 s[0:1], 0, v52
	s_nop 1
	v_cndmask_b32_e64 v34, v34, v50, s[0:1]
	v_cmp_lt_f32_e64 s[0:1], 0, v53
	s_nop 1
	v_cndmask_b32_e64 v34, v34, v51, s[0:1]
	v_mul_f32_e32 v50, 0x37800000, v34
	v_cndmask_b32_e32 v34, v34, v50, vcc
	v_cmp_class_f32_e32 vcc, v1, v49
	s_nop 1
	v_cndmask_b32_e32 v1, v34, v1, vcc
	v_div_scale_f32 v34, s[0:1], v1, v1, 1.0
	v_rcp_f32_e32 v51, v34
	v_div_scale_f32 v50, vcc, 1.0, v1, 1.0
	v_fma_f32 v52, -v34, v51, 1.0
	v_fmac_f32_e32 v51, v52, v51
	v_mul_f32_e32 v52, v50, v51
	v_fma_f32 v53, -v34, v52, v50
	v_fmac_f32_e32 v52, v53, v51
	v_fma_f32 v34, -v34, v52, v50
	v_div_fmas_f32 v34, v34, v51, v52
	v_div_fixup_f32 v34, v34, v1, 1.0
	v_pk_mul_f32 v[6:7], v[6:7], v[34:35] op_sel_hi:[1,0]
	v_pk_mul_f32 v[8:9], v[8:9], v[34:35] op_sel_hi:[1,0]
	v_pk_mul_f32 v[50:51], v[2:3], v[34:35] op_sel_hi:[1,0]
	v_pk_mul_f32 v[52:53], v[4:5], v[34:35] op_sel_hi:[1,0]
	v_pk_mul_f32 v[14:15], v[14:15], v[34:35] op_sel_hi:[1,0]
	v_pk_mul_f32 v[16:17], v[16:17], v[34:35] op_sel_hi:[1,0]
	v_pk_mul_f32 v[10:11], v[10:11], v[34:35] op_sel_hi:[1,0]
	v_pk_mul_f32 v[12:13], v[12:13], v[34:35] op_sel_hi:[1,0]
	v_pk_mul_f32 v[22:23], v[22:23], v[34:35] op_sel_hi:[1,0]
	v_pk_mul_f32 v[24:25], v[24:25], v[34:35] op_sel_hi:[1,0]
	v_pk_mul_f32 v[18:19], v[18:19], v[34:35] op_sel_hi:[1,0]
	v_pk_mul_f32 v[20:21], v[20:21], v[34:35] op_sel_hi:[1,0]
	v_pk_mul_f32 v[30:31], v[30:31], v[34:35] op_sel_hi:[1,0]
	v_pk_mul_f32 v[32:33], v[32:33], v[34:35] op_sel_hi:[1,0]
	v_pk_mul_f32 v[26:27], v[26:27], v[34:35] op_sel_hi:[1,0]
	v_pk_mul_f32 v[28:29], v[28:29], v[34:35] op_sel_hi:[1,0]
	v_cvt_pk_bf16_f32 v2, v6, v7
	v_cvt_pk_bf16_f32 v3, v8, v9
	v_cvt_pk_bf16_f32 v4, v50, v51
	v_cvt_pk_bf16_f32 v5, v52, v53
	v_cvt_pk_bf16_f32 v6, v14, v15
	v_cvt_pk_bf16_f32 v7, v16, v17
	v_cvt_pk_bf16_f32 v8, v10, v11
	v_cvt_pk_bf16_f32 v9, v12, v13
	v_cvt_pk_bf16_f32 v10, v22, v23
	v_cvt_pk_bf16_f32 v11, v24, v25
	v_cvt_pk_bf16_f32 v12, v18, v19
	v_cvt_pk_bf16_f32 v13, v20, v21
	v_cvt_pk_bf16_f32 v14, v30, v31
	v_cvt_pk_bf16_f32 v15, v32, v33
	v_cvt_pk_bf16_f32 v16, v26, v27
	v_cvt_pk_bf16_f32 v17, v28, v29
	global_store_dwordx4 v[40:41], v[2:5], off
	global_store_dwordx4 v[40:41], v[6:9], off offset:1024
	global_store_dwordx4 v[40:41], v[10:13], off offset:2048
	global_store_dwordx4 v[40:41], v[14:17], off offset:3072
	v_lshl_add_u64 v[40:41], v[40:41], 0, s[14:15]
	s_cbranch_scc1 .LBB0_975

.LBB0_1303:
	s_lshl_b32 s8, s77, 4
	s_add_i32 s6, s76, s8
	s_ashr_i32 s7, s6, 31
	s_lshl_b64 s[12:13], s[6:7], 13
	v_lshl_add_u64 v[34:35], v[128:129], 0, s[12:13]
	v_lshl_add_u64 v[36:37], v[34:35], 0, s[56:57]
	v_add_co_u32_e32 v36, vcc, 0x1000, v34
	v_and_b32_e32 v1, 64, v220
	s_nop 0
	v_addc_co_u32_e32 v37, vcc, 0, v35, vcc
	v_lshl_add_u64 v[34:35], v[34:35], 0, s[54:55]
	v_xor_b32_e32 v34, 1, v220
	v_add_u32_e32 v1, 64, v1
	s_or_b32 s6, s6, 1
	v_cmp_lt_i32_e32 vcc, v34, v1
	s_ashr_i32 s7, s6, 31
	s_lshl_b64 s[6:7], s[6:7], 13
	v_cndmask_b32_e32 v34, v220, v34, vcc
	v_lshlrev_b32_e32 v225, 2, v34
	v_lshl_add_u64 v[34:35], v[128:129], 0, s[6:7]
	v_add_co_u32_e32 v70, vcc, s70, v34
	v_lshl_add_u64 v[36:37], v[34:35], 0, s[54:55]
	s_nop 0
	v_addc_co_u32_e32 v71, vcc, 0, v35, vcc
	v_lshl_add_u64 v[72:73], v[34:35], 0, s[56:57]
	s_nop 0
	s_add_i32 s8, s8, s75
	s_add_i32 s60, s8, s2
	s_ashr_i32 s61, s60, 31
	s_add_i32 s62, s8, s33
	s_ashr_i32 s63, s62, 31
	s_waitcnt vmcnt(13)
	v_mov_b32_e32 v76, v119
	s_waitcnt vmcnt(12)
	v_mov_b32_e32 v77, v115
	v_mov_b32_e32 v80, v121
	v_mov_b32_e32 v81, v117
	v_mov_b32_e32 v74, v118
	v_mov_b32_e32 v75, v114
	v_mov_b32_e32 v78, v120
	v_mov_b32_e32 v79, v116
	s_waitcnt vmcnt(11)
	v_pk_mul_f32 v[82:83], v[112:113], v[112:113]
	v_pk_mul_f32 v[84:85], v[110:111], v[110:111]
	v_pk_mul_f32 v[76:77], v[76:77], v[76:77]
	v_pk_mul_f32 v[80:81], v[80:81], v[80:81]
	v_pk_mov_b32 v[94:95], v[84:85], v[82:83] op_sel:[1,0]
	v_mov_b32_e32 v85, v83
	v_pk_fma_f32 v[74:75], v[74:75], v[74:75], v[76:77]
	v_pk_fma_f32 v[76:77], v[78:79], v[78:79], v[80:81]
	s_waitcnt vmcnt(10)
	v_mul_f32_e32 v86, v107, v107
	v_mul_f32_e32 v88, v109, v109
	v_pk_add_f32 v[78:79], v[94:95], v[84:85]
	v_pk_add_f32 v[74:75], v[74:75], v[76:77]
	v_pk_fma_f32 v[82:83], v[106:107], v[106:107], v[86:87] op_sel_hi:[1,1,0]
	v_pk_fma_f32 v[86:87], v[108:109], v[108:109], v[88:89] op_sel_hi:[1,1,0]
	s_waitcnt vmcnt(8)
	v_mul_f32_e32 v95, v90, v90
	v_mul_f32_e32 v100, v91, v91
	v_pk_add_f32 v[76:77], v[78:79], v[78:79] op_sel:[0,1] op_sel_hi:[1,0]
	v_pk_add_f32 v[74:75], v[74:75], v[74:75] op_sel:[0,1] op_sel_hi:[1,0]
	v_mul_f32_e32 v83, v92, v92
	v_mul_f32_e32 v87, v93, v93
	s_waitcnt vmcnt(7)
	v_pk_mul_f32 v[80:81], v[68:69], v[68:69]
	v_pk_mul_f32 v[84:85], v[66:67], v[66:67]
	v_mov_b32_e32 v77, v100
	v_mov_b32_e32 v75, v95
	v_pk_mov_b32 v[78:79], v[84:85], v[80:81] op_sel:[1,0]
	v_mov_b32_e32 v85, v81
	v_pk_add_f32 v[82:83], v[82:83], v[86:87]
	v_pk_add_f32 v[74:75], v[74:75], v[76:77]
	s_waitcnt vmcnt(6)
	v_mul_f32_e32 v88, v63, v63
	v_mul_f32_e32 v94, v65, v65
	v_pk_add_f32 v[78:79], v[78:79], v[84:85]
	v_pk_add_f32 v[74:75], v[74:75], v[82:83]
	v_mul_f32_e32 v96, v58, v58
	v_mul_f32_e32 v97, v59, v59
	v_mul_f32_e32 v98, v60, v60
	v_mul_f32_e32 v99, v61, v61
	v_pk_fma_f32 v[80:81], v[62:63], v[62:63], v[88:89] op_sel_hi:[1,1,0]
	v_pk_fma_f32 v[88:89], v[64:65], v[64:65], v[94:95] op_sel_hi:[1,1,0]
	v_pk_add_f32 v[78:79], v[78:79], v[78:79] op_sel:[0,1] op_sel_hi:[1,0]
	v_pk_add_f32 v[74:75], v[74:75], v[74:75] op_sel:[0,1] op_sel_hi:[1,0]
	v_mov_b32_e32 v81, v98
	v_mov_b32_e32 v79, v97
	v_mov_b32_e32 v75, v96
	v_mov_b32_e32 v89, v99
	v_pk_add_f32 v[74:75], v[74:75], v[78:79]
	v_pk_add_f32 v[76:77], v[80:81], v[88:89]
	s_waitcnt vmcnt(0)
	v_mov_b32_e32 v42, v196
	v_mov_b32_e32 v43, v197
	v_mov_b32_e32 v44, v198
	v_mov_b32_e32 v45, v199
	v_mov_b32_e32 v46, v200
	v_mov_b32_e32 v47, v201
	v_mov_b32_e32 v48, v202
	v_mov_b32_e32 v49, v203
	v_mov_b32_e32 v38, v204
	v_mov_b32_e32 v39, v205
	v_mov_b32_e32 v40, v206
	v_mov_b32_e32 v41, v207
	v_mov_b32_e32 v34, v208
	v_mov_b32_e32 v35, v209
	v_mov_b32_e32 v36, v210
	v_mov_b32_e32 v37, v211
	v_mov_b32_e32 v98, v212
	v_mov_b32_e32 v99, v213
	v_mov_b32_e32 v100, v214
	v_mov_b32_e32 v101, v215
	global_load_dwordx4 v[82:85], v[126:127], off
	global_load_dwordx4 v[86:89], v[126:127], off offset:256
	v_pk_add_f32 v[74:75], v[74:75], v[76:77]
	v_xor_b32_e32 v76, 2, v220
	v_add_f32_e32 v74, v74, v75
	s_nop 1
	v_mov_b32_dpp v75, v74 quad_perm:[1,0,3,2] row_mask:0xf bank_mask:0xf
	s_nop 1
	v_cmp_lt_i32_e32 vcc, v76, v1
	s_waitcnt lgkmcnt(0)
	v_add_f32_e32 v74, v74, v75
	v_cndmask_b32_e32 v76, v220, v76, vcc
	v_lshlrev_b32_e32 v230, 2, v76
	s_nop 1
	v_mov_b32_dpp v75, v74 quad_perm:[2,3,0,1] row_mask:0xf bank_mask:0xf
	s_nop 1
	v_xor_b32_e32 v76, 4, v220
	v_cmp_lt_i32_e32 vcc, v76, v1
	s_waitcnt lgkmcnt(0)
	v_add_f32_e32 v74, v74, v75
	v_cndmask_b32_e32 v76, v220, v76, vcc
	v_lshlrev_b32_e32 v231, 2, v76
	s_nop 1
	v_mov_b32_dpp v75, v74 row_half_mirror row_mask:0xf bank_mask:0xf
	s_nop 1
	v_xor_b32_e32 v76, 8, v220
	v_cmp_lt_i32_e32 vcc, v76, v1
	s_waitcnt lgkmcnt(0)
	v_add_f32_e32 v74, v74, v75
	v_cndmask_b32_e32 v76, v220, v76, vcc
	v_lshlrev_b32_e32 v232, 2, v76
	s_nop 1
	v_mov_b32_dpp v75, v74 row_mirror row_mask:0xf bank_mask:0xf
	s_nop 1
	v_xor_b32_e32 v76, 16, v220
	v_cmp_lt_i32_e32 vcc, v76, v1
	s_waitcnt lgkmcnt(0)
	v_add_f32_e32 v74, v74, v75
	v_cndmask_b32_e32 v76, v220, v76, vcc
	v_lshlrev_b32_e32 v233, 2, v76
	ds_bpermute_b32 v75, v233, v74
	v_xor_b32_e32 v76, 32, v220
	v_cmp_lt_i32_e32 vcc, v76, v1
	s_waitcnt lgkmcnt(0)
	v_add_f32_e32 v74, v74, v75
	v_cndmask_b32_e32 v1, v220, v76, vcc
	v_lshlrev_b32_e32 v1, 2, v1
	ds_bpermute_b32 v75, v1, v74
	s_waitcnt lgkmcnt(0)
	v_add_f32_e32 v70, v74, v75
	v_fmamk_f32 v70, v70, 0x3a000000, v221
	v_mul_f32_e32 v71, 0x4f800000, v70
	v_cmp_gt_f32_e32 vcc, s71, v70
	s_nop 1
	v_cndmask_b32_e32 v124, v70, v71, vcc
	v_sqrt_f32_e32 v216, v124
	global_load_dwordx4 v[94:97], v[126:127], off offset:512
	global_load_dwordx4 v[70:73], v[126:127], off offset:3072
	global_load_dwordx4 v[74:77], v[126:127], off offset:3328
	global_load_dwordx4 v[78:81], v[126:127], off offset:3584
	v_add_u32_e32 v217, -1, v216
	v_fma_f32 v226, -v217, v216, v124
	v_cmp_ge_f32_e64 s[6:7], 0, v226
	v_add_u32_e32 v226, 1, v216
	s_nop 0
	v_cndmask_b32_e64 v217, v216, v217, s[6:7]
	v_fma_f32 v216, -v226, v216, v124
	v_cmp_lt_f32_e64 s[6:7], 0, v216
	s_nop 1
	v_cndmask_b32_e64 v216, v217, v226, s[6:7]
	v_mul_f32_e32 v217, 0x37800000, v216
	v_cndmask_b32_e32 v216, v216, v217, vcc
	v_cmp_class_f32_e32 vcc, v124, v222
	s_nop 1
	v_cndmask_b32_e32 v124, v216, v124, vcc
	v_div_scale_f32 v216, s[6:7], v124, v124, 1.0
	v_rcp_f32_e32 v217, v216
	s_lshl_b64 s[6:7], s[60:61], 12
	v_fma_f32 v226, -v216, v217, 1.0
	v_fmac_f32_e32 v217, v226, v217
	v_div_scale_f32 v226, vcc, 1.0, v124, 1.0
	v_mul_f32_e32 v227, v226, v217
	v_fma_f32 v228, -v216, v227, v226
	v_fmac_f32_e32 v227, v228, v217
	v_fma_f32 v216, -v216, v227, v226
	v_div_fmas_f32 v216, v216, v217, v227
	v_div_fixup_f32 v124, v216, v124, 1.0
	v_pk_mul_f32 v[118:119], v[118:119], v[124:125] op_sel_hi:[1,0]
	v_pk_mul_f32 v[120:121], v[120:121], v[124:125] op_sel_hi:[1,0]
	v_pk_mul_f32 v[114:115], v[114:115], v[124:125] op_sel_hi:[1,0]
	v_pk_mul_f32 v[116:117], v[116:117], v[124:125] op_sel_hi:[1,0]
	v_pk_mul_f32 v[120:121], v[28:29], v[120:121]
	v_pk_mul_f32 v[118:119], v[26:27], v[118:119]
	v_pk_mul_f32 v[116:117], v[4:5], v[116:117]
	v_pk_mul_f32 v[114:115], v[2:3], v[114:115]
	v_lshl_add_u64 v[216:217], v[130:131], 0, s[6:7]
	v_cvt_pk_bf16_f32 v226, v118, v119
	v_cvt_pk_bf16_f32 v227, v120, v121
	v_cvt_pk_bf16_f32 v228, v114, v115
	v_cvt_pk_bf16_f32 v229, v116, v117
	v_pk_mul_f32 v[110:111], v[110:111], v[124:125] op_sel_hi:[1,0]
	v_pk_mul_f32 v[112:113], v[112:113], v[124:125] op_sel_hi:[1,0]
	v_pk_mul_f32 v[106:107], v[106:107], v[124:125] op_sel_hi:[1,0]
	v_pk_mul_f32 v[108:109], v[108:109], v[124:125] op_sel_hi:[1,0]
	global_store_dwordx4 v[216:217], v[226:229], off
	v_pk_mul_f32 v[112:113], v[8:9], v[112:113]
	v_pk_mul_f32 v[110:111], v[6:7], v[110:111]
	v_add_u32_e32 v226, s26, v122
	v_pk_mul_f32 v[108:109], v[12:13], v[108:109]
	v_pk_mul_f32 v[106:107], v[10:11], v[106:107]
	ds_write_b128 v226, v[118:121]
	ds_write_b128 v226, v[114:117] offset:16
	v_cvt_pk_bf16_f32 v114, v110, v111
	v_cvt_pk_bf16_f32 v115, v112, v113
	v_cvt_pk_bf16_f32 v116, v106, v107
	v_cvt_pk_bf16_f32 v117, v108, v109
	global_store_dwordx4 v[216:217], v[114:117], off offset:1024
	ds_write_b128 v226, v[110:113] offset:2048
	ds_write_b128 v226, v[106:109] offset:2064
	s_waitcnt vmcnt(15)
	v_mov_b32_e32 v108, v55
	s_waitcnt vmcnt(14)
	v_mov_b32_e32 v109, v51
	v_mov_b32_e32 v106, v54
	v_mov_b32_e32 v107, v50
	v_pk_mul_f32 v[108:109], v[108:109], v[108:109]
	v_mov_b32_e32 v110, v57
	v_mov_b32_e32 v111, v53
	v_pk_fma_f32 v[106:107], v[106:107], v[106:107], v[108:109]
	v_mov_b32_e32 v108, v56
	v_mov_b32_e32 v109, v52
	v_pk_mul_f32 v[110:111], v[110:111], v[110:111]
	v_pk_mul_f32 v[90:91], v[90:91], v[124:125] op_sel_hi:[1,0]
	v_pk_fma_f32 v[108:109], v[108:109], v[108:109], v[110:111]
	s_waitcnt vmcnt(12)
	v_pk_mul_f32 v[110:111], v[46:47], v[46:47]
	v_pk_add_f32 v[106:107], v[106:107], v[108:109]
	v_pk_mul_f32 v[108:109], v[48:49], v[48:49]
	v_pk_add_f32 v[106:107], v[106:107], v[106:107] op_sel:[0,1] op_sel_hi:[1,0]
	v_pk_mov_b32 v[112:113], v[110:111], v[108:109] op_sel:[1,0]
	v_mov_b32_e32 v111, v109
	v_pk_add_f32 v[108:109], v[112:113], v[110:111]
	s_waitcnt vmcnt(11)
	v_mul_f32_e32 v110, v38, v38
	v_mul_f32_e32 v111, v39, v39
	v_pk_add_f32 v[108:109], v[108:109], v[108:109] op_sel:[0,1] op_sel_hi:[1,0]
	v_mov_b32_e32 v107, v110
	v_mov_b32_e32 v109, v111
	v_pk_add_f32 v[106:107], v[106:107], v[108:109]
	v_mul_f32_e32 v108, v43, v43
	v_mul_f32_e32 v110, v45, v45
	v_mul_f32_e32 v112, v40, v40
	v_mul_f32_e32 v113, v41, v41
	v_pk_fma_f32 v[108:109], v[42:43], v[42:43], v[108:109] op_sel_hi:[1,1,0]
	v_pk_fma_f32 v[110:111], v[44:45], v[44:45], v[110:111] op_sel_hi:[1,1,0]
	v_mov_b32_e32 v109, v112
	v_mov_b32_e32 v111, v113
	v_pk_add_f32 v[108:109], v[108:109], v[110:111]
	s_waitcnt vmcnt(10)
	v_pk_mul_f32 v[110:111], v[34:35], v[34:35]
	v_pk_add_f32 v[106:107], v[106:107], v[108:109]
	v_pk_mul_f32 v[108:109], v[36:37], v[36:37]
	v_pk_add_f32 v[106:107], v[106:107], v[106:107] op_sel:[0,1] op_sel_hi:[1,0]
	v_pk_mov_b32 v[112:113], v[110:111], v[108:109] op_sel:[1,0]
	v_mov_b32_e32 v111, v109
	v_pk_add_f32 v[108:109], v[112:113], v[110:111]
	s_waitcnt vmcnt(8)
	v_mul_f32_e32 v110, v98, v98
	v_mul_f32_e32 v111, v99, v99
	v_pk_add_f32 v[108:109], v[108:109], v[108:109] op_sel:[0,1] op_sel_hi:[1,0]
	v_mov_b32_e32 v107, v110
	v_mov_b32_e32 v109, v111
	v_pk_add_f32 v[106:107], v[106:107], v[108:109]
	v_mul_f32_e32 v108, v103, v103
	v_mul_f32_e32 v110, v105, v105
	v_mul_f32_e32 v112, v100, v100
	v_mul_f32_e32 v113, v101, v101
	v_pk_fma_f32 v[108:109], v[102:103], v[102:103], v[108:109] op_sel_hi:[1,1,0]
	v_pk_fma_f32 v[110:111], v[104:105], v[104:105], v[110:111] op_sel_hi:[1,1,0]
	v_mov_b32_e32 v109, v112
	v_mov_b32_e32 v111, v113
	v_pk_add_f32 v[108:109], v[108:109], v[110:111]
	v_pk_mul_f32 v[92:93], v[92:93], v[124:125] op_sel_hi:[1,0]
	v_pk_add_f32 v[106:107], v[106:107], v[108:109]
	v_pk_mul_f32 v[66:67], v[66:67], v[124:125] op_sel_hi:[1,0]
	v_add_f32_e32 v106, v106, v107
	s_nop 1
	v_mov_b32_dpp v107, v106 quad_perm:[1,0,3,2] row_mask:0xf bank_mask:0xf
	s_nop 1
	v_pk_mul_f32 v[68:69], v[68:69], v[124:125] op_sel_hi:[1,0]
	v_pk_mul_f32 v[92:93], v[20:21], v[92:93]
	v_pk_mul_f32 v[90:91], v[18:19], v[90:91]
	v_pk_mul_f32 v[68:69], v[16:17], v[68:69]
	s_waitcnt lgkmcnt(0)
	v_add_f32_e32 v107, v106, v107
	s_nop 1
	v_mov_b32_dpp v108, v107 quad_perm:[2,3,0,1] row_mask:0xf bank_mask:0xf
	s_nop 1
	v_pk_mul_f32 v[66:67], v[14:15], v[66:67]
	v_cvt_pk_bf16_f32 v106, v90, v91
	v_cvt_pk_bf16_f32 v109, v68, v69
	v_pk_mul_f32 v[62:63], v[62:63], v[124:125] op_sel_hi:[1,0]
	s_waitcnt lgkmcnt(0)
	v_add_f32_e32 v110, v107, v108
	s_nop 1
	v_mov_b32_dpp v111, v110 row_half_mirror row_mask:0xf bank_mask:0xf
	s_nop 1
	v_cvt_pk_bf16_f32 v107, v92, v93
	v_cvt_pk_bf16_f32 v108, v66, v67
	global_store_dwordx4 v[216:217], v[106:109], off offset:2048
	ds_write_b128 v226, v[90:93] offset:4096
	ds_write_b128 v226, v[66:69] offset:4112
	s_waitcnt lgkmcnt(2)
	v_add_f32_e32 v106, v110, v111
	s_nop 1
	v_mov_b32_dpp v107, v106 row_mirror row_mask:0xf bank_mask:0xf
	s_nop 1
	v_pk_mul_f32 v[64:65], v[64:65], v[124:125] op_sel_hi:[1,0]
	v_pk_mul_f32 v[58:59], v[58:59], v[124:125] op_sel_hi:[1,0]
	v_pk_mul_f32 v[60:61], v[60:61], v[124:125] op_sel_hi:[1,0]
	v_pk_mul_f32 v[64:65], v[24:25], v[64:65]
	s_waitcnt lgkmcnt(0)
	v_add_f32_e32 v66, v106, v107
	ds_bpermute_b32 v67, v233, v66
	v_pk_mul_f32 v[62:63], v[22:23], v[62:63]
	v_pk_mul_f32 v[60:61], v[32:33], v[60:61]
	v_pk_mul_f32 v[58:59], v[30:31], v[58:59]
	v_cvt_pk_bf16_f32 v69, v60, v61
	s_waitcnt lgkmcnt(0)
	v_add_f32_e32 v68, v66, v67
	ds_bpermute_b32 v1, v1, v68
	v_cvt_pk_bf16_f32 v66, v62, v63
	v_cvt_pk_bf16_f32 v67, v64, v65
	s_waitcnt lgkmcnt(0)
	v_add_f32_e32 v1, v68, v1
	v_fmamk_f32 v1, v1, 0x3a000000, v221
	v_mul_f32_e32 v68, 0x4f800000, v1
	v_cmp_gt_f32_e32 vcc, s71, v1
	s_nop 1
	v_cndmask_b32_e32 v1, v1, v68, vcc
	v_sqrt_f32_e32 v90, v1
	v_cvt_pk_bf16_f32 v68, v58, v59
	global_store_dwordx4 v[216:217], v[66:69], off offset:3072
	ds_write_b128 v226, v[62:65] offset:6144
	ds_write_b128 v226, v[58:61] offset:6160
	v_add_u32_e32 v66, -1, v90
	v_fma_f32 v67, -v66, v90, v1
	v_cmp_ge_f32_e64 s[6:7], 0, v67
	v_add_u32_e32 v67, 1, v90
	v_fma_f32 v68, -v67, v90, v1
	v_cndmask_b32_e64 v66, v90, v66, s[6:7]
	v_cmp_lt_f32_e64 s[6:7], 0, v68
	s_nop 1
	v_cndmask_b32_e64 v66, v66, v67, s[6:7]
	v_mul_f32_e32 v67, 0x37800000, v66
	v_cndmask_b32_e32 v66, v66, v67, vcc
	v_cmp_class_f32_e32 vcc, v1, v222
	s_nop 1
	v_cndmask_b32_e32 v1, v66, v1, vcc
	v_div_scale_f32 v66, s[6:7], v1, v1, 1.0
	v_rcp_f32_e32 v67, v66
	s_lshl_b64 s[6:7], s[62:63], 12
	v_lshl_add_u64 v[64:65], v[130:131], 0, s[6:7]
	v_fma_f32 v58, -v66, v67, 1.0
	v_fmac_f32_e32 v67, v58, v67
	v_div_scale_f32 v58, vcc, 1.0, v1, 1.0
	v_mul_f32_e32 v59, v58, v67
	v_fma_f32 v60, -v66, v59, v58
	v_fmac_f32_e32 v59, v60, v67
	v_fma_f32 v58, -v66, v59, v58
	v_div_fmas_f32 v58, v58, v67, v59
	v_div_fixup_f32 v62, v58, v1, 1.0
	v_pk_mul_f32 v[54:55], v[54:55], v[62:63] op_sel_hi:[1,0]
	v_pk_mul_f32 v[56:57], v[56:57], v[62:63] op_sel_hi:[1,0]
	v_pk_mul_f32 v[50:51], v[50:51], v[62:63] op_sel_hi:[1,0]
	v_pk_mul_f32 v[52:53], v[52:53], v[62:63] op_sel_hi:[1,0]
	v_pk_mul_f32 v[56:57], v[28:29], v[56:57]
	v_pk_mul_f32 v[54:55], v[26:27], v[54:55]
	v_pk_mul_f32 v[52:53], v[4:5], v[52:53]
	v_pk_mul_f32 v[50:51], v[2:3], v[50:51]
	v_pk_mul_f32 v[46:47], v[46:47], v[62:63] op_sel_hi:[1,0]
	v_pk_mul_f32 v[48:49], v[48:49], v[62:63] op_sel_hi:[1,0]
	v_pk_mul_f32 v[42:43], v[42:43], v[62:63] op_sel_hi:[1,0]
	v_pk_mul_f32 v[44:45], v[44:45], v[62:63] op_sel_hi:[1,0]
	v_cvt_pk_bf16_f32 v58, v54, v55
	v_cvt_pk_bf16_f32 v59, v56, v57
	v_cvt_pk_bf16_f32 v60, v50, v51
	v_cvt_pk_bf16_f32 v61, v52, v53
	v_add_u32_e32 v1, s34, v122
	v_pk_mul_f32 v[48:49], v[8:9], v[48:49]
	v_pk_mul_f32 v[46:47], v[6:7], v[46:47]
	v_pk_mul_f32 v[44:45], v[12:13], v[44:45]
	v_pk_mul_f32 v[42:43], v[10:11], v[42:43]
	v_pk_mul_f32 v[38:39], v[38:39], v[62:63] op_sel_hi:[1,0]
	v_pk_mul_f32 v[40:41], v[40:41], v[62:63] op_sel_hi:[1,0]
	v_pk_mul_f32 v[34:35], v[34:35], v[62:63] op_sel_hi:[1,0]
	v_pk_mul_f32 v[36:37], v[36:37], v[62:63] op_sel_hi:[1,0]
	global_store_dwordx4 v[64:65], v[58:61], off
	ds_write_b128 v1, v[54:57]
	ds_write_b128 v1, v[50:53] offset:16
	v_cvt_pk_bf16_f32 v50, v46, v47
	v_cvt_pk_bf16_f32 v51, v48, v49
	v_cvt_pk_bf16_f32 v52, v42, v43
	v_cvt_pk_bf16_f32 v53, v44, v45
	v_pk_mul_f32 v[40:41], v[20:21], v[40:41]
	v_pk_mul_f32 v[38:39], v[18:19], v[38:39]
	v_pk_mul_f32 v[36:37], v[16:17], v[36:37]
	v_pk_mul_f32 v[34:35], v[14:15], v[34:35]
	global_store_dwordx4 v[64:65], v[50:53], off offset:1024
	ds_write_b128 v1, v[46:49] offset:2048
	ds_write_b128 v1, v[42:45] offset:2064
	v_cvt_pk_bf16_f32 v42, v38, v39
	v_cvt_pk_bf16_f32 v43, v40, v41
	v_cvt_pk_bf16_f32 v44, v34, v35
	v_cvt_pk_bf16_f32 v45, v36, v37
	global_store_dwordx4 v[64:65], v[42:45], off offset:2048
	ds_write_b128 v1, v[38:41] offset:4096
	ds_write_b128 v1, v[34:37] offset:4112
	v_pk_mul_f32 v[34:35], v[102:103], v[62:63] op_sel_hi:[1,0]
	v_pk_mul_f32 v[36:37], v[104:105], v[62:63] op_sel_hi:[1,0]
	v_pk_mul_f32 v[38:39], v[98:99], v[62:63] op_sel_hi:[1,0]
	v_pk_mul_f32 v[40:41], v[100:101], v[62:63] op_sel_hi:[1,0]
	v_pk_mul_f32 v[36:37], v[24:25], v[36:37]
	v_pk_mul_f32 v[34:35], v[22:23], v[34:35]
	v_pk_mul_f32 v[40:41], v[32:33], v[40:41]
	v_pk_mul_f32 v[38:39], v[30:31], v[38:39]
	v_cvt_pk_bf16_f32 v42, v34, v35
	v_cvt_pk_bf16_f32 v43, v36, v37
	v_cvt_pk_bf16_f32 v44, v38, v39
	v_cvt_pk_bf16_f32 v45, v40, v41
	global_store_dwordx4 v[64:65], v[42:45], off offset:3072
	ds_write_b128 v1, v[34:37] offset:6144
	ds_write_b128 v1, v[38:41] offset:6160
	s_waitcnt lgkmcnt(0)
	s_barrier
	v_add_u32_e32 v216, 0x1800, v255
	global_load_dwordx4 v[132:135], v216, s[94:95]
	v_add_u32_e32 v216, 0x1900, v255
	global_load_dwordx4 v[136:139], v216, s[94:95]
	v_add_u32_e32 v216, 0x1a00, v255
	global_load_dwordx4 v[140:143], v216, s[94:95]
	v_add_u32_e32 v216, 0x2400, v255
	global_load_dwordx4 v[144:147], v216, s[94:95]
	v_add_u32_e32 v216, 0x2500, v255
	global_load_dwordx4 v[148:151], v216, s[94:95]
	v_add_u32_e32 v216, 0x2600, v255
	global_load_dwordx4 v[152:155], v216, s[94:95]
	v_add_u32_e32 v216, 0x3000, v255
	global_load_dwordx4 v[156:159], v216, s[94:95]
	v_add_u32_e32 v216, 0x3100, v255
	global_load_dwordx4 v[160:163], v216, s[94:95]
	v_add_u32_e32 v216, 0x3200, v255
	global_load_dwordx4 v[164:167], v216, s[94:95]
	v_add_u32_e32 v216, 0x3c00, v255
	global_load_dwordx4 v[168:171], v216, s[94:95]
	v_add_u32_e32 v216, 0x3d00, v255
	global_load_dwordx4 v[172:175], v216, s[94:95]
	v_add_u32_e32 v216, 0x3e00, v255
	global_load_dwordx4 v[176:179], v216, s[94:95]
	v_add_u32_e32 v216, 0x4800, v255
	global_load_dwordx4 v[180:183], v216, s[94:95]
	v_add_u32_e32 v216, 0x4900, v255
	global_load_dwordx4 v[184:187], v216, s[94:95]
	v_add_u32_e32 v216, 0x4a00, v255
	global_load_dwordx4 v[188:191], v216, s[94:95]
	v_add_u32_e32 v216, 0x5400, v255
	global_load_dwordx4 v[192:195], v216, s[94:95]
	v_add_u32_e32 v216, 0x5500, v255
	global_load_dwordx4 v[226:229], v216, s[94:95]
	v_add_u32_e32 v216, 0x5600, v255
	global_load_dwordx4 v[230:233], v216, s[94:95]
	ds_read_b128 v[234:237], v123
	ds_read_b128 v[238:241], v123 offset:64
	s_waitcnt vmcnt(31) lgkmcnt(1)
	v_mfma_f32_16x16x4_f32 v[242:245], v234, v82, 0
	s_waitcnt vmcnt(30)
	v_mfma_f32_16x16x4_f32 v[246:249], v234, v86, 0
	s_waitcnt vmcnt(29)
	v_mfma_f32_16x16x4_f32 v[250:253], v234, v94, 0
	v_mfma_f32_16x16x4_f32 v[242:245], v235, v83, v[242:245]
	v_mfma_f32_16x16x4_f32 v[246:249], v235, v87, v[246:249]
	v_mfma_f32_16x16x4_f32 v[250:253], v235, v95, v[250:253]
	v_mfma_f32_16x16x4_f32 v[242:245], v236, v84, v[242:245]
	v_mfma_f32_16x16x4_f32 v[246:249], v236, v88, v[246:249]
	v_mfma_f32_16x16x4_f32 v[250:253], v236, v96, v[250:253]
	v_mfma_f32_16x16x4_f32 v[82:85], v237, v85, v[242:245]
	v_mfma_f32_16x16x4_f32 v[86:89], v237, v89, v[246:249]
	v_mfma_f32_16x16x4_f32 v[94:97], v237, v97, v[250:253]
	s_waitcnt vmcnt(28) lgkmcnt(0)
	v_mfma_f32_16x16x4_f32 v[82:85], v238, v70, v[82:85]
	s_waitcnt vmcnt(27)
	v_mfma_f32_16x16x4_f32 v[86:89], v238, v74, v[86:89]
	s_waitcnt vmcnt(26)
	v_mfma_f32_16x16x4_f32 v[94:97], v238, v78, v[94:97]
	v_mfma_f32_16x16x4_f32 v[82:85], v239, v71, v[82:85]
	v_mfma_f32_16x16x4_f32 v[86:89], v239, v75, v[86:89]
	v_mfma_f32_16x16x4_f32 v[94:97], v239, v79, v[94:97]
	v_mfma_f32_16x16x4_f32 v[82:85], v240, v72, v[82:85]
	v_mfma_f32_16x16x4_f32 v[86:89], v240, v76, v[86:89]
	v_mfma_f32_16x16x4_f32 v[94:97], v240, v80, v[94:97]
	v_mfma_f32_16x16x4_f32 v[70:73], v241, v73, v[82:85]
	v_mfma_f32_16x16x4_f32 v[74:77], v241, v77, v[86:89]
	s_nop 5
	ds_read_b128 v[82:85], v123 offset:128
	ds_read_b128 v[86:89], v123 offset:192
	v_mfma_f32_16x16x4_f32 v[78:81], v241, v81, v[94:97]
	s_waitcnt vmcnt(17) lgkmcnt(1)
	v_mfma_f32_16x16x4_f32 v[70:73], v82, v132, v[70:73]
	s_waitcnt vmcnt(16)
	v_mfma_f32_16x16x4_f32 v[74:77], v82, v136, v[74:77]
	s_waitcnt vmcnt(15)
	v_mfma_f32_16x16x4_f32 v[78:81], v82, v140, v[78:81]
	v_mfma_f32_16x16x4_f32 v[70:73], v83, v133, v[70:73]
	v_mfma_f32_16x16x4_f32 v[74:77], v83, v137, v[74:77]
	v_mfma_f32_16x16x4_f32 v[78:81], v83, v141, v[78:81]
	v_mfma_f32_16x16x4_f32 v[70:73], v84, v134, v[70:73]
	v_mfma_f32_16x16x4_f32 v[74:77], v84, v138, v[74:77]
	v_mfma_f32_16x16x4_f32 v[78:81], v84, v142, v[78:81]
	v_mfma_f32_16x16x4_f32 v[132:135], v85, v135, v[70:73]
	v_mfma_f32_16x16x4_f32 v[136:139], v85, v139, v[74:77]
	v_mfma_f32_16x16x4_f32 v[140:143], v85, v143, v[78:81]
	s_waitcnt vmcnt(12) lgkmcnt(0)
	v_mfma_f32_16x16x4_f32 v[140:143], v86, v152, v[140:143]
	v_mfma_f32_16x16x4_f32 v[132:135], v86, v144, v[132:135]
	v_mfma_f32_16x16x4_f32 v[136:139], v86, v148, v[136:139]
	v_mfma_f32_16x16x4_f32 v[140:143], v87, v153, v[140:143]
	v_mfma_f32_16x16x4_f32 v[132:135], v87, v145, v[132:135]
	v_mfma_f32_16x16x4_f32 v[136:139], v87, v149, v[136:139]
	v_mfma_f32_16x16x4_f32 v[140:143], v88, v154, v[140:143]
	v_mfma_f32_16x16x4_f32 v[132:135], v88, v146, v[132:135]
	v_mfma_f32_16x16x4_f32 v[136:139], v88, v150, v[136:139]
	v_mfma_f32_16x16x4_f32 v[132:135], v89, v147, v[132:135]
	v_add_u32_e32 v216, 0x6000, v255
	global_load_dwordx4 v[144:147], v216, s[94:95]
	v_add_u32_e32 v216, 0x6100, v255
	global_load_dwordx4 v[70:73], v216, s[94:95]
	v_add_u32_e32 v216, 0x6200, v255
	global_load_dwordx4 v[74:77], v216, s[94:95]
	v_add_u32_e32 v216, 0x6c00, v255
	global_load_dwordx4 v[78:81], v216, s[94:95]
	v_mfma_f32_16x16x4_f32 v[136:139], v89, v151, v[136:139]
	v_add_u32_e32 v216, 0x6d00, v255
	global_load_dwordx4 v[148:151], v216, s[94:95]
	v_add_u32_e32 v216, 0x6e00, v255
	global_load_dwordx4 v[82:85], v216, s[94:95]
	v_add_u32_e32 v216, 0x7800, v255
	global_load_dwordx4 v[94:97], v216, s[94:95]
	v_add_u32_e32 v216, 0x7900, v255
	global_load_dwordx4 v[234:237], v216, s[94:95]
	v_add_u32_e32 v216, 0x7a00, v255
	global_load_dwordx4 v[238:241], v216, s[94:95]
	v_add_u32_e32 v216, 0x8400, v255
	global_load_dwordx4 v[242:245], v216, s[94:95]
	v_add_u32_e32 v216, 0x8500, v255
	global_load_dwordx4 v[246:249], v216, s[94:95]
	v_add_u32_e32 v216, 0x8600, v255
	global_load_dwordx4 v[250:253], v216, s[94:95]
	v_mfma_f32_16x16x4_f32 v[140:143], v89, v155, v[140:143]
	ds_read_b128 v[152:155], v123 offset:256
	ds_read_b128 v[86:89], v123 offset:320
	s_waitcnt vmcnt(23) lgkmcnt(1)
	v_mfma_f32_16x16x4_f32 v[132:135], v152, v156, v[132:135]
	s_waitcnt vmcnt(22)
	v_mfma_f32_16x16x4_f32 v[136:139], v152, v160, v[136:139]
	s_waitcnt vmcnt(21)
	v_mfma_f32_16x16x4_f32 v[140:143], v152, v164, v[140:143]
	v_mfma_f32_16x16x4_f32 v[132:135], v153, v157, v[132:135]
	v_mfma_f32_16x16x4_f32 v[136:139], v153, v161, v[136:139]
	v_mfma_f32_16x16x4_f32 v[140:143], v153, v165, v[140:143]
	v_mfma_f32_16x16x4_f32 v[132:135], v154, v158, v[132:135]
	v_mfma_f32_16x16x4_f32 v[136:139], v154, v162, v[136:139]
	v_mfma_f32_16x16x4_f32 v[140:143], v154, v166, v[140:143]
	v_mfma_f32_16x16x4_f32 v[132:135], v155, v159, v[132:135]
	v_mfma_f32_16x16x4_f32 v[136:139], v155, v163, v[136:139]
	v_mfma_f32_16x16x4_f32 v[140:143], v155, v167, v[140:143]
	ds_read_b128 v[152:155], v123 offset:384
	ds_read_b128 v[156:159], v123 offset:448
	s_waitcnt vmcnt(20) lgkmcnt(2)
	v_mfma_f32_16x16x4_f32 v[132:135], v86, v168, v[132:135]
	s_waitcnt vmcnt(19)
	v_mfma_f32_16x16x4_f32 v[136:139], v86, v172, v[136:139]
	s_waitcnt vmcnt(18)
	v_mfma_f32_16x16x4_f32 v[140:143], v86, v176, v[140:143]
	v_mfma_f32_16x16x4_f32 v[132:135], v87, v169, v[132:135]
	v_mfma_f32_16x16x4_f32 v[136:139], v87, v173, v[136:139]
	v_mfma_f32_16x16x4_f32 v[140:143], v87, v177, v[140:143]
	v_mfma_f32_16x16x4_f32 v[132:135], v88, v170, v[132:135]
	v_mfma_f32_16x16x4_f32 v[136:139], v88, v174, v[136:139]
	v_mfma_f32_16x16x4_f32 v[140:143], v88, v178, v[140:143]
	v_mfma_f32_16x16x4_f32 v[132:135], v89, v171, v[132:135]
	v_mfma_f32_16x16x4_f32 v[136:139], v89, v175, v[136:139]
	v_mfma_f32_16x16x4_f32 v[140:143], v89, v179, v[140:143]
	s_waitcnt vmcnt(17) lgkmcnt(1)
	v_mfma_f32_16x16x4_f32 v[132:135], v152, v180, v[132:135]
	s_waitcnt vmcnt(16)
	v_mfma_f32_16x16x4_f32 v[136:139], v152, v184, v[136:139]
	s_waitcnt vmcnt(15)
	v_mfma_f32_16x16x4_f32 v[140:143], v152, v188, v[140:143]
	v_mfma_f32_16x16x4_f32 v[132:135], v153, v181, v[132:135]
	v_mfma_f32_16x16x4_f32 v[136:139], v153, v185, v[136:139]
	v_mfma_f32_16x16x4_f32 v[140:143], v153, v189, v[140:143]
	v_mfma_f32_16x16x4_f32 v[132:135], v154, v182, v[132:135]
	v_mfma_f32_16x16x4_f32 v[136:139], v154, v186, v[136:139]
	v_mfma_f32_16x16x4_f32 v[140:143], v154, v190, v[140:143]
	v_mfma_f32_16x16x4_f32 v[132:135], v155, v183, v[132:135]
	v_mfma_f32_16x16x4_f32 v[136:139], v155, v187, v[136:139]
	v_mfma_f32_16x16x4_f32 v[140:143], v155, v191, v[140:143]
	v_add_u32_e32 v216, 0x9000, v255
	global_load_dwordx4 v[152:155], v216, s[94:95]
	v_add_u32_e32 v216, 0x9100, v255
	global_load_dwordx4 v[160:163], v216, s[94:95]
	v_add_u32_e32 v216, 0x9200, v255
	global_load_dwordx4 v[164:167], v216, s[94:95]
	v_add_u32_e32 v216, 0x9c00, v255
	global_load_dwordx4 v[86:89], v216, s[94:95]
	s_waitcnt vmcnt(16) lgkmcnt(0)
	v_mfma_f32_16x16x4_f32 v[140:143], v156, v230, v[140:143]
	v_mfma_f32_16x16x4_f32 v[132:135], v156, v192, v[132:135]
	v_mfma_f32_16x16x4_f32 v[136:139], v156, v226, v[136:139]
	v_mfma_f32_16x16x4_f32 v[140:143], v157, v231, v[140:143]
	v_mfma_f32_16x16x4_f32 v[132:135], v157, v193, v[132:135]
	v_mfma_f32_16x16x4_f32 v[136:139], v157, v227, v[136:139]
	v_mfma_f32_16x16x4_f32 v[140:143], v158, v232, v[140:143]
	v_mfma_f32_16x16x4_f32 v[132:135], v158, v194, v[132:135]
	v_mfma_f32_16x16x4_f32 v[136:139], v158, v228, v[136:139]
	v_mfma_f32_16x16x4_f32 v[132:135], v159, v195, v[132:135]
	v_mfma_f32_16x16x4_f32 v[136:139], v159, v229, v[136:139]
	v_add_u32_e32 v216, 0x9d00, v255
	global_load_dwordx4 v[168:171], v216, s[94:95]
	v_add_u32_e32 v216, 0x9e00, v255
	global_load_dwordx4 v[172:175], v216, s[94:95]
	v_add_u32_e32 v216, 0xa800, v255
	global_load_dwordx4 v[176:179], v216, s[94:95]
	v_add_u32_e32 v216, 0xa900, v255
	global_load_dwordx4 v[180:183], v216, s[94:95]
	v_add_u32_e32 v216, 0xaa00, v255
	global_load_dwordx4 v[184:187], v216, s[94:95]
	v_add_u32_e32 v216, 0xb400, v255
	global_load_dwordx4 v[188:191], v216, s[94:95]
	v_add_u32_e32 v216, 0xb500, v255
	global_load_dwordx4 v[192:195], v216, s[94:95]
	v_add_u32_e32 v216, 0xb600, v255
	global_load_dwordx4 v[226:229], v216, s[94:95]
	s_add_i32 s82, s77, 1
	s_min_u32 s82, s82, 3
	s_lshl_b32 s82, s82, 4
	s_add_i32 s82, s76, s82
	s_ashr_i32 s83, s82, 31
	s_lshl_b64 s[82:83], s[82:83], 13
	v_lshl_add_u64 v[98:99], v[128:129], 0, s[82:83]
	s_add_u32 s82, s82, 0x1000
	s_addc_u32 s83, s83, 0
	global_load_dwordx4 v[118:121], v[98:99], off
	global_load_dwordx4 v[114:117], v[98:99], off offset:16
	global_load_dwordx4 v[110:113], v[98:99], off offset:2048
	global_load_dwordx4 v[106:109], v[98:99], off offset:2064
	v_lshl_add_u64 v[100:101], v[128:129], 0, s[82:83]
	s_add_u32 s82, s82, 0x1000
	s_addc_u32 s83, s83, 0
	global_load_dwordx4 v[58:61], v[100:101], off offset:2064
	global_load_dwordx4 v[90:93], v[100:101], off
	global_load_dwordx4 v[66:69], v[100:101], off offset:16
	global_load_dwordx4 v[62:65], v[100:101], off offset:2048
	v_lshl_add_u64 v[98:99], v[128:129], 0, s[82:83]
	s_nop 0
	global_load_dwordx4 v[54:57], v[98:99], off
	global_load_dwordx4 v[50:53], v[98:99], off offset:16
	global_load_dwordx4 v[196:199], v[98:99], off offset:2064
	global_load_dwordx4 v[200:203], v[98:99], off offset:2048
	s_add_u32 s82, s82, 0x1000
	s_addc_u32 s83, s83, 0
	v_lshl_add_u64 v[100:101], v[128:129], 0, s[82:83]
	s_nop 0
	global_load_dwordx4 v[204:207], v[100:101], off
	global_load_dwordx4 v[208:211], v[100:101], off offset:16
	global_load_dwordx4 v[102:105], v[100:101], off offset:2048
	global_load_dwordx4 v[212:215], v[100:101], off offset:2064
	v_mfma_f32_16x16x4_f32 v[140:143], v159, v233, v[140:143]
	ds_read_b128 v[156:159], v123 offset:512
	ds_read_b128 v[230:233], v123 offset:576
	s_waitcnt vmcnt(39) lgkmcnt(1)
	v_mfma_f32_16x16x4_f32 v[132:135], v156, v144, v[132:135]
	s_waitcnt vmcnt(38)
	v_mfma_f32_16x16x4_f32 v[136:139], v156, v70, v[136:139]
	s_waitcnt vmcnt(37)
	v_mfma_f32_16x16x4_f32 v[140:143], v156, v74, v[140:143]
	v_mfma_f32_16x16x4_f32 v[132:135], v157, v145, v[132:135]
	v_mfma_f32_16x16x4_f32 v[136:139], v157, v71, v[136:139]
	v_mfma_f32_16x16x4_f32 v[140:143], v157, v75, v[140:143]
	v_mfma_f32_16x16x4_f32 v[132:135], v158, v146, v[132:135]
	v_mfma_f32_16x16x4_f32 v[136:139], v158, v72, v[136:139]
	v_mfma_f32_16x16x4_f32 v[140:143], v158, v76, v[140:143]
	v_mfma_f32_16x16x4_f32 v[132:135], v159, v147, v[132:135]
	v_mfma_f32_16x16x4_f32 v[136:139], v159, v73, v[136:139]
	v_mfma_f32_16x16x4_f32 v[140:143], v159, v77, v[140:143]
	s_waitcnt vmcnt(36) lgkmcnt(0)
	v_mfma_f32_16x16x4_f32 v[132:135], v230, v78, v[132:135]
	s_waitcnt vmcnt(35)
	v_mfma_f32_16x16x4_f32 v[136:139], v230, v148, v[136:139]
	s_waitcnt vmcnt(34)
	v_mfma_f32_16x16x4_f32 v[140:143], v230, v82, v[140:143]
	v_mfma_f32_16x16x4_f32 v[132:135], v231, v79, v[132:135]
	v_mfma_f32_16x16x4_f32 v[136:139], v231, v149, v[136:139]
	v_mfma_f32_16x16x4_f32 v[140:143], v231, v83, v[140:143]
	v_mfma_f32_16x16x4_f32 v[132:135], v232, v80, v[132:135]
	v_mfma_f32_16x16x4_f32 v[136:139], v232, v150, v[136:139]
	v_mfma_f32_16x16x4_f32 v[140:143], v232, v84, v[140:143]
	v_mfma_f32_16x16x4_f32 v[132:135], v233, v81, v[132:135]
	v_mfma_f32_16x16x4_f32 v[136:139], v233, v151, v[136:139]
	ds_read_b128 v[144:147], v123 offset:640
	ds_read_b128 v[148:151], v123 offset:704
	v_mfma_f32_16x16x4_f32 v[140:143], v233, v85, v[140:143]
	s_waitcnt vmcnt(33) lgkmcnt(1)
	v_mfma_f32_16x16x4_f32 v[132:135], v144, v94, v[132:135]
	s_waitcnt vmcnt(32)
	v_mfma_f32_16x16x4_f32 v[136:139], v144, v234, v[136:139]
	s_waitcnt vmcnt(31)
	v_mfma_f32_16x16x4_f32 v[140:143], v144, v238, v[140:143]
	v_mfma_f32_16x16x4_f32 v[132:135], v145, v95, v[132:135]
	v_mfma_f32_16x16x4_f32 v[136:139], v145, v235, v[136:139]
	v_mfma_f32_16x16x4_f32 v[140:143], v145, v239, v[140:143]
	v_mfma_f32_16x16x4_f32 v[132:135], v146, v96, v[132:135]
	v_mfma_f32_16x16x4_f32 v[136:139], v146, v236, v[136:139]
	v_mfma_f32_16x16x4_f32 v[140:143], v146, v240, v[140:143]
	v_mfma_f32_16x16x4_f32 v[132:135], v147, v97, v[132:135]
	v_mfma_f32_16x16x4_f32 v[136:139], v147, v237, v[136:139]
	v_mfma_f32_16x16x4_f32 v[140:143], v147, v241, v[140:143]
	s_waitcnt vmcnt(30) lgkmcnt(0)
	v_mfma_f32_16x16x4_f32 v[132:135], v148, v242, v[132:135]
	s_waitcnt vmcnt(29)
	v_mfma_f32_16x16x4_f32 v[136:139], v148, v246, v[136:139]
	s_waitcnt vmcnt(28)
	v_mfma_f32_16x16x4_f32 v[140:143], v148, v250, v[140:143]
	v_mfma_f32_16x16x4_f32 v[132:135], v149, v243, v[132:135]
	v_mfma_f32_16x16x4_f32 v[136:139], v149, v247, v[136:139]
	v_mfma_f32_16x16x4_f32 v[140:143], v149, v251, v[140:143]
	v_mfma_f32_16x16x4_f32 v[132:135], v150, v244, v[132:135]
	v_mfma_f32_16x16x4_f32 v[136:139], v150, v248, v[136:139]
	v_mfma_f32_16x16x4_f32 v[140:143], v150, v252, v[140:143]
	v_mfma_f32_16x16x4_f32 v[132:135], v151, v245, v[132:135]
	v_mfma_f32_16x16x4_f32 v[136:139], v151, v249, v[136:139]
	v_mfma_f32_16x16x4_f32 v[140:143], v151, v253, v[140:143]
	ds_read_b128 v[144:147], v123 offset:768
	ds_read_b128 v[148:151], v123 offset:832
	s_waitcnt vmcnt(27) lgkmcnt(1)
	v_mfma_f32_16x16x4_f32 v[132:135], v144, v152, v[132:135]
	s_waitcnt vmcnt(26)
	v_mfma_f32_16x16x4_f32 v[136:139], v144, v160, v[136:139]
	s_waitcnt vmcnt(25)
	v_mfma_f32_16x16x4_f32 v[140:143], v144, v164, v[140:143]
	v_mfma_f32_16x16x4_f32 v[132:135], v145, v153, v[132:135]
	v_mfma_f32_16x16x4_f32 v[136:139], v145, v161, v[136:139]
	v_mfma_f32_16x16x4_f32 v[140:143], v145, v165, v[140:143]
	v_mfma_f32_16x16x4_f32 v[132:135], v146, v154, v[132:135]
	v_mfma_f32_16x16x4_f32 v[136:139], v146, v162, v[136:139]
	v_mfma_f32_16x16x4_f32 v[140:143], v146, v166, v[140:143]
	v_mfma_f32_16x16x4_f32 v[132:135], v147, v155, v[132:135]
	v_mfma_f32_16x16x4_f32 v[136:139], v147, v163, v[136:139]
	v_mfma_f32_16x16x4_f32 v[140:143], v147, v167, v[140:143]
	s_waitcnt vmcnt(24) lgkmcnt(0)
	v_mfma_f32_16x16x4_f32 v[132:135], v148, v86, v[132:135]
	s_waitcnt vmcnt(23)
	v_mfma_f32_16x16x4_f32 v[136:139], v148, v168, v[136:139]
	s_waitcnt vmcnt(22)
	v_mfma_f32_16x16x4_f32 v[140:143], v148, v172, v[140:143]
	v_mfma_f32_16x16x4_f32 v[132:135], v149, v87, v[132:135]
	v_mfma_f32_16x16x4_f32 v[136:139], v149, v169, v[136:139]
	v_mfma_f32_16x16x4_f32 v[140:143], v149, v173, v[140:143]
	v_mfma_f32_16x16x4_f32 v[132:135], v150, v88, v[132:135]
	v_mfma_f32_16x16x4_f32 v[136:139], v150, v170, v[136:139]
	v_mfma_f32_16x16x4_f32 v[140:143], v150, v174, v[140:143]
	v_mfma_f32_16x16x4_f32 v[132:135], v151, v89, v[132:135]
	v_mfma_f32_16x16x4_f32 v[136:139], v151, v171, v[136:139]
	v_mfma_f32_16x16x4_f32 v[140:143], v151, v175, v[140:143]
	ds_read_b128 v[144:147], v123 offset:896
	ds_read_b128 v[148:151], v123 offset:960
	s_waitcnt vmcnt(21) lgkmcnt(1)
	v_mfma_f32_16x16x4_f32 v[132:135], v144, v176, v[132:135]
	s_waitcnt vmcnt(20)
	v_mfma_f32_16x16x4_f32 v[136:139], v144, v180, v[136:139]
	s_waitcnt vmcnt(19)
	v_mfma_f32_16x16x4_f32 v[140:143], v144, v184, v[140:143]
	v_mfma_f32_16x16x4_f32 v[132:135], v145, v177, v[132:135]
	v_mfma_f32_16x16x4_f32 v[136:139], v145, v181, v[136:139]
	v_mfma_f32_16x16x4_f32 v[140:143], v145, v185, v[140:143]
	v_mfma_f32_16x16x4_f32 v[132:135], v146, v178, v[132:135]
	v_mfma_f32_16x16x4_f32 v[136:139], v146, v182, v[136:139]
	v_mfma_f32_16x16x4_f32 v[140:143], v146, v186, v[140:143]
	v_mfma_f32_16x16x4_f32 v[132:135], v147, v179, v[132:135]
	v_mfma_f32_16x16x4_f32 v[136:139], v147, v183, v[136:139]
	v_mfma_f32_16x16x4_f32 v[140:143], v147, v187, v[140:143]
	s_waitcnt vmcnt(18) lgkmcnt(0)
	v_mfma_f32_16x16x4_f32 v[132:135], v148, v188, v[132:135]
	s_waitcnt vmcnt(17)
	v_mfma_f32_16x16x4_f32 v[136:139], v148, v192, v[136:139]
	s_waitcnt vmcnt(16)
	v_mfma_f32_16x16x4_f32 v[140:143], v148, v226, v[140:143]
	v_mfma_f32_16x16x4_f32 v[132:135], v149, v189, v[132:135]
	v_mfma_f32_16x16x4_f32 v[136:139], v149, v193, v[136:139]
	v_mfma_f32_16x16x4_f32 v[140:143], v149, v227, v[140:143]
	v_mfma_f32_16x16x4_f32 v[132:135], v150, v190, v[132:135]
	v_mfma_f32_16x16x4_f32 v[136:139], v150, v194, v[136:139]
	v_mfma_f32_16x16x4_f32 v[140:143], v150, v228, v[140:143]
	v_mfma_f32_16x16x4_f32 v[132:135], v151, v191, v[132:135]
	v_mfma_f32_16x16x4_f32 v[136:139], v151, v195, v[136:139]
	v_mfma_f32_16x16x4_f32 v[140:143], v151, v229, v[140:143]
	s_nop 8
	ds_write2_b32 v223, v132, v136 offset1:16
	ds_write2_b32 v223, v140, v133 offset0:32 offset1:48
	ds_write2_b32 v223, v137, v141 offset0:64 offset1:80
	ds_write2_b32 v223, v134, v138 offset0:96 offset1:112
	ds_write2_b32 v223, v142, v135 offset0:128 offset1:144
	ds_write2_b32 v223, v139, v143 offset0:160 offset1:176
	s_waitcnt lgkmcnt(0)
	s_barrier
	s_and_saveexec_b64 s[6:7], s[4:5]
	s_cbranch_execz .LBB0_1306
	s_mov_b64 s[8:9], 0
	v_mov_b32_e32 v34, v0
